# v26 + P3 attention loops: K tile staged before barrier 1 (its LDS buffer is already free), second per-tile barrier removed (one barrier per KV tile)
# speedup vs baseline: 1.0099x; 1.0099x over previous
; #define LAS __attribute__((address_space(3)))
; __device__ __forceinline__ void finishSM(f32x16& p0, f32x16& p1, float alpha, float& l_reg, bf16x8& pa0, bf16x8& pa1, bf16x8& pa2, bf16x8& pa3) {
; #pragma unroll
;     for (int r = 0; r < 16; ++r) p1[r] = __builtin_amdgcn_exp2f(p1[r]);
;     float ps = 0;
; #pragma unroll
;     for (int r = 0; r < 16; ++r) ps += p0[r];
; #pragma unroll
;     for (int r = 0; r < 16; ++r) ps += p1[r];
;     { auto rr = __builtin_amdgcn_permlane32_swap(__float_as_uint(ps), __float_as_uint(ps), false, false);
;       ps = __uint_as_float(rr[0]) + __uint_as_float(rr[1]); }
;     l_reg = l_reg * alpha + ps;
;     ...
;     PK4(p0, 0, pa0); PK4(p0, 8, pa1); PK4(p1, 0, pa2); PK4(p1, 8, pa3);
;     ...
; }
; template <int MODE>
; __device__ __forceinline__ void qkt(f32x16& p0, f32x16& p1, const LAS unsigned char* Ks, const bf16x8* qr, const LAS unsigned char* Qs, int r32, int hi, int cbase) {
;     p0 = f32x16{}; p1 = f32x16{};
; #pragma unroll
;     for (int d0 = 0; d0 < Cfg<MODE>::ND; ++d0) { const int cb = cbase + (d0 * 16 + hi * 8) * 2;
;         const bf16x8 b0 = *(const LAS bf16x8*)(Ks + KSWZ(r32, cb));
;         const bf16x8 b1 = *(const LAS bf16x8*)(Ks + KSWZ(32 + r32, cb));
;         bf16x8 q; if constexpr (MODE == 0) q = *(const LAS bf16x8*)(Qs + KSWZ(r32, cb)); else q = qr[d0];
;         p0 = __builtin_amdgcn_mfma_f32_32x32x16_bf16(b0, q, p0, 0, 0, 0);
;         p1 = __builtin_amdgcn_mfma_f32_32x32x16_bf16(b1, q, p1, 0, 0, 0); }
; }
; __device__ __forceinline__ int v_st(int k, int c) { const int kk = (k & ~0xC) | ((k & 4) << 1) | ((k & 8) >> 1); return ((kk >> 3) * 4 + (c >> 5)) * 512 + ((kk & 7) * 32 + (c & 31)) * 2; }
; __device__ __forceinline__ int v_rd_base(int lane) { return ((lane & 3) << 3) | (((lane >> 2) & 3) << 6) | (((lane >> 4) & 1) << 5) | (((lane >> 5) & 1) << 8); }
; template <int OFF> __device__ __forceinline__ s16x4 tr_read(int vb) {
;     s16x4 r; asm volatile("ds_read_b64_tr_b16 %0, %1 offset:%2" : "=&v"(r) : "v"(vb), "i"(OFF) : "memory"); return r;
; }
; template <int D0> __device__ __forceinline__ void pv_one(f32x16& od, int vb, bf16x8 pa0, bf16x8 pa1, bf16x8 pa2, bf16x8 pa3) {
;     const s16x4 l0 = tr_read<v_rd_off(D0, 0, 0)>(vb), h0 = tr_read<v_rd_off(D0, 0, 1)>(vb), l1 = tr_read<v_rd_off(D0, 1, 0)>(vb), h1 = tr_read<v_rd_off(D0, 1, 1)>(vb);
.LBB0_412:
	ds_read_b128 v[68:71], v204 offset:49152
	ds_read_b128 v[72:75], v204 offset:57344
	ds_read_b128 v[224:227], v195 offset:49152
	ds_read_b128 v[228:231], v195 offset:57344
	ds_read_b128 v[232:235], v205 offset:49152
	ds_read_b128 v[236:239], v205 offset:57344
	s_waitcnt lgkmcnt(5)
	v_mfma_f32_32x32x16_bf16 v[82:97], v[68:71], v[110:113], 0
	v_exp_f32_e32 v141, v66
	v_exp_f32_e32 v248, v67
	v_exp_f32_e32 v132, v132
	v_exp_f32_e32 v133, v133
	v_exp_f32_e32 v130, v130
	v_exp_f32_e32 v131, v131
	v_exp_f32_e32 v128, v128
	s_waitcnt lgkmcnt(3)
	v_mfma_f32_32x32x16_bf16 v[82:97], v[224:227], v[106:109], v[82:97]
	v_add_f32_e32 v224, 0, v201
	v_add_f32_e32 v224, v203, v224
	v_add_f32_e32 v224, v153, v224
	v_add_f32_e32 v224, v202, v224
	v_add_f32_e32 v224, v151, v224
	v_add_f32_e32 v224, v200, v224
	v_add_f32_e32 v224, v150, v224
	v_mfma_f32_32x32x16_bf16 v[66:81], v[72:75], v[110:113], 0
	v_add_f32_e32 v224, v152, v224
	v_add_f32_e32 v224, v147, v224
	v_add_f32_e32 v224, v149, v224
	v_add_f32_e32 v224, v145, v224
	v_add_f32_e32 v224, v148, v224
	v_add_f32_e32 v224, v143, v224
	v_add_f32_e32 v224, v146, v224
	s_waitcnt lgkmcnt(2)
	v_mfma_f32_32x32x16_bf16 v[66:81], v[228:231], v[106:109], v[66:81]
	v_add_f32_e32 v224, v142, v224
	v_add_f32_e32 v224, v144, v224
	v_add_f32_e32 v224, v132, v224
	v_add_f32_e32 v224, v133, v224
	v_add_f32_e32 v224, v141, v224
	v_exp_f32_e32 v129, v129
	v_add_f32_e32 v224, v248, v224
	s_waitcnt lgkmcnt(1)
	v_mfma_f32_32x32x16_bf16 v[82:97], v[232:235], v[102:105], v[82:97]
	v_exp_f32_e32 v126, v126
	v_add_f32_e32 v224, v130, v224
	ds_read_b128 v[240:243], v206 offset:49152
	ds_read_b128 v[244:247], v206 offset:57344
	v_exp_f32_e32 v127, v127
	v_add_f32_e32 v224, v131, v224
	v_exp_f32_e32 v138, v138
	v_add_f32_e32 v224, v128, v224
	s_waitcnt lgkmcnt(2)
	v_mfma_f32_32x32x16_bf16 v[66:81], v[236:239], v[102:105], v[66:81]
	v_exp_f32_e32 v139, v139
	v_add_f32_e32 v224, v129, v224
	v_exp_f32_e32 v136, v136
	v_add_f32_e32 v224, v126, v224
	v_exp_f32_e32 v137, v137
	v_add_f32_e32 v224, v127, v224
	v_exp_f32_e32 v134, v134
	s_waitcnt lgkmcnt(1)
	v_mfma_f32_32x32x16_bf16 v[82:97], v[240:243], v[98:101], v[82:97]
	v_add_f32_e32 v224, v138, v224
	v_exp_f32_e32 v135, v135
	v_add_f32_e32 v224, v139, v224
	v_add_f32_e32 v224, v136, v224
	v_add_f32_e32 v224, v137, v224
	v_add_f32_e32 v224, v134, v224
	v_add_f32_e32 v224, v135, v224
	s_waitcnt lgkmcnt(0)
	v_mfma_f32_32x32x16_bf16 v[66:81], v[244:247], v[98:101], v[66:81]
	v_mov_b32_e32 v225, v224
	v_cvt_pk_bf16_f32 v226, v201, v203
	v_cvt_pk_bf16_f32 v227, v153, v202
	v_cvt_pk_bf16_f32 v228, v151, v200
	s_nop 1
	v_permlane32_swap_b32_e32 v224, v225
	v_cvt_pk_bf16_f32 v229, v150, v152
	v_permlane32_swap_b32_e32 v226, v228
	v_cvt_pk_bf16_f32 v150, v147, v149
	v_cvt_pk_bf16_f32 v151, v145, v148
	v_cvt_pk_bf16_f32 v152, v143, v146
	v_cvt_pk_bf16_f32 v153, v142, v144
	v_cvt_pk_bf16_f32 v142, v132, v133
	v_cvt_pk_bf16_f32 v143, v141, v248
	v_cvt_pk_bf16_f32 v144, v130, v131
	v_cvt_pk_bf16_f32 v145, v128, v129
	v_cvt_pk_bf16_f32 v146, v126, v127
	v_cvt_pk_bf16_f32 v147, v138, v139
	v_cvt_pk_bf16_f32 v148, v136, v137
	v_cvt_pk_bf16_f32 v149, v134, v135
	v_permlane32_swap_b32_e32 v227, v229
	v_permlane32_swap_b32_e32 v150, v152
	v_permlane32_swap_b32_e32 v151, v153
	v_permlane32_swap_b32_e32 v142, v144
	v_permlane32_swap_b32_e32 v143, v145
	v_permlane32_swap_b32_e32 v146, v148
	v_permlane32_swap_b32_e32 v147, v149
	v_lshl_add_u64 v[200:201], v[196:197], 0, s[20:21]
	v_add_co_u32_e32 v126, vcc, s43, v200
	v_lshl_add_u64 v[202:203], v[198:199], 0, s[20:21]
	s_nop 0
	v_addc_co_u32_e32 v127, vcc, 0, v201, vcc
	v_add_co_u32_e32 v130, vcc, s45, v200
	s_nop 1
	v_addc_co_u32_e32 v131, vcc, 0, v201, vcc
	v_add_co_u32_e32 v134, vcc, s57, v202
	global_load_dwordx4 v[126:129], v[126:127], off
	s_nop 0
	global_load_dwordx4 v[130:133], v[130:131], off
	v_addc_co_u32_e32 v135, vcc, 0, v203, vcc
	global_load_dwordx4 v[134:137], v[134:135], off
	ds_read_b64_tr_b16 v[230:231], v175 offset:0
	ds_read_b64_tr_b16 v[232:233], v175 offset:0x800
	ds_read_b64_tr_b16 v[234:235], v175 offset:0x1000
	ds_read_b64_tr_b16 v[236:237], v175 offset:0x1800
	ds_read_b64_tr_b16 v[238:239], v175 offset:0x2000
	ds_read_b64_tr_b16 v[240:241], v175 offset:0x2800
	ds_read_b64_tr_b16 v[242:243], v175 offset:0x3000
	ds_read_b64_tr_b16 v[244:245], v175 offset:0x3800
	s_waitcnt lgkmcnt(0)
	s_nop 0
	v_mfma_f32_32x32x16_bf16 v[2:17], v[226:229], v[230:233], v[2:17]
	ds_read_b64_tr_b16 v[230:231], v175 offset:0x200
	ds_read_b64_tr_b16 v[232:233], v175 offset:0xa00
	v_mfma_f32_32x32x16_bf16 v[2:17], v[150:153], v[234:237], v[2:17]
	ds_read_b64_tr_b16 v[234:235], v175 offset:0x1200
	ds_read_b64_tr_b16 v[236:237], v175 offset:0x1a00
	v_mfma_f32_32x32x16_bf16 v[2:17], v[142:145], v[238:241], v[2:17]
	ds_read_b64_tr_b16 v[238:239], v175 offset:0x2200
	ds_read_b64_tr_b16 v[240:241], v175 offset:0x2a00
	ds_read_b64_tr_b16 v[246:247], v175 offset:0x3200
	ds_read_b64_tr_b16 v[248:249], v175 offset:0x3a00
	s_waitcnt lgkmcnt(0)
	v_mfma_f32_32x32x16_bf16 v[2:17], v[146:149], v[242:245], v[2:17]
	v_mfma_f32_32x32x16_bf16 v[50:65], v[226:229], v[230:233], v[50:65]
	ds_read_b64_tr_b16 v[230:231], v175 offset:0x400
	ds_read_b64_tr_b16 v[232:233], v175 offset:0xc00
	v_mfma_f32_32x32x16_bf16 v[50:65], v[150:153], v[234:237], v[50:65]
	ds_read_b64_tr_b16 v[234:235], v175 offset:0x1400
	ds_read_b64_tr_b16 v[236:237], v175 offset:0x1c00
	v_mfma_f32_32x32x16_bf16 v[50:65], v[142:145], v[238:241], v[50:65]
	ds_read_b64_tr_b16 v[238:239], v175 offset:0x2400
	ds_read_b64_tr_b16 v[240:241], v175 offset:0x2c00
	ds_read_b64_tr_b16 v[242:243], v175 offset:0x3400
	ds_read_b64_tr_b16 v[244:245], v175 offset:0x3c00
	s_waitcnt lgkmcnt(0)
; #define SWAIT() do { if constexpr (MODE == 1) asm volatile("s_waitcnt vmcnt(3)" ::: "memory"); else asm volatile("s_waitcnt vmcnt(4)" ::: "memory"); } while (0)
; #define RESC(a) do { if (__any((a) < 1.f)) { if (hi == 0) al_l[r32] = (a); asm volatile("s_waitcnt lgkmcnt(0)" ::: "memory"); \
;     _Pragma("unroll") for (int d = 0; d < 4; ++d) _Pragma("unroll") for (int r = 0; r < 16; ++r) o[d][r] *= al_l[crow(r, hi)]; } } while (0)
; template <int MODE>
; __device__ __forceinline__ void partialSM(f32x16& p0, f32x16& p1, float& m_reg, float& mn, float& alpha) {
;     constexpr float SCALE = Cfg<MODE>::SCALE, C = SCALE * 1.4426950408889634f;
;     float pmax = p0[0];
; #pragma unroll
;     for (int r = 1; r < 16; ++r) pmax = fmaxf(pmax, p0[r]);
; #pragma unroll
;     for (int r = 0; r < 16; ++r) pmax = fmaxf(pmax, p1[r]);
;     { auto rr = __builtin_amdgcn_permlane32_swap(__float_as_uint(pmax), __float_as_uint(pmax), false, false);
;       pmax = fmaxf(__uint_as_float(rr[0]), __uint_as_float(rr[1])); }
;     if (__builtin_expect(__all(pmax - m_reg <= THR / SCALE), 1)) { mn = m_reg; alpha = 1.f; }
;     else { mn = fmaxf(m_reg, pmax); alpha = __builtin_amdgcn_exp2f((m_reg - mn) * C); m_reg = mn; }
; template <int MODE>
; __device__ __forceinline__ void attn_pass(const bf16_t* __restrict__ Qb, const bf16_t* __restrict__ Kh, const bf16_t* __restrict__ Vh, const int NT, const int kr0, const int g4, const int map,
;                                           LAS unsigned char* lds, f32x16 (&o)[4]) {
;     ...
;         pv_d0(o, vb0, pa0, pa1, pa2, pa3); partialSM<MODE>(pB0, pB1, m_reg, mnB, alB);
;         __syncthreads(); SWAIT(); SWRITE(0, SE);
;         RESC(alB); __syncthreads();
	v_mfma_f32_32x32x16_bf16 v[50:65], v[146:149], v[246:249], v[50:65]
	v_mfma_f32_32x32x16_bf16 v[34:49], v[226:229], v[230:233], v[34:49]
	ds_read_b64_tr_b16 v[230:231], v175 offset:0x600
	ds_read_b64_tr_b16 v[232:233], v175 offset:0xe00
	v_mfma_f32_32x32x16_bf16 v[34:49], v[150:153], v[234:237], v[34:49]
	ds_read_b64_tr_b16 v[234:235], v175 offset:0x1600
	ds_read_b64_tr_b16 v[236:237], v175 offset:0x1e00
	v_mfma_f32_32x32x16_bf16 v[34:49], v[142:145], v[238:241], v[34:49]
	ds_read_b64_tr_b16 v[238:239], v175 offset:0x2600
	ds_read_b64_tr_b16 v[240:241], v175 offset:0x2e00
	ds_read_b64_tr_b16 v[246:247], v175 offset:0x3600
	ds_read_b64_tr_b16 v[248:249], v175 offset:0x3e00
	s_waitcnt lgkmcnt(0)
	v_mfma_f32_32x32x16_bf16 v[34:49], v[146:149], v[242:245], v[34:49]
	v_mfma_f32_32x32x16_bf16 v[18:33], v[226:229], v[230:233], v[18:33]
	v_max_f32_e32 v138, v83, v83
	v_max_f32_e32 v139, v82, v82
	v_max_f32_e32 v138, v139, v138
	v_max3_f32 v138, v138, v84, v85
	v_max3_f32 v138, v138, v86, v87
	v_max3_f32 v138, v138, v88, v89
	v_max3_f32 v138, v138, v90, v91
	v_max3_f32 v138, v138, v92, v93
	v_mfma_f32_32x32x16_bf16 v[18:33], v[150:153], v[234:237], v[18:33]
	v_max3_f32 v138, v138, v94, v95
	v_max3_f32 v138, v138, v96, v97
	v_max3_f32 v138, v138, v66, v67
	v_max3_f32 v138, v138, v68, v69
	v_max3_f32 v138, v138, v70, v71
	v_max3_f32 v138, v138, v72, v73
	v_max3_f32 v138, v138, v74, v75
	v_max3_f32 v138, v138, v76, v77
	v_mfma_f32_32x32x16_bf16 v[18:33], v[142:145], v[238:241], v[18:33]
	v_max3_f32 v138, v138, v78, v79
	v_max3_f32 v138, v138, v80, v81
	v_mov_b32_e32 v139, v138
	s_nop 1
	v_permlane32_swap_b32_e32 v138, v139
	v_max_f32_e32 v139, v139, v139
	v_max_f32_e32 v138, v138, v138
	v_max_f32_e32 v138, v138, v139
	v_max_f32_e32 v141, v140, v140
	v_sub_f32_e32 v139, v138, v140
	v_max_f32_e32 v138, v141, v138
	v_mfma_f32_32x32x16_bf16 v[18:33], v[146:149], v[246:249], v[18:33]
	v_sub_f32_e32 v141, v140, v138
	v_mul_f32_e32 v141, 0x3e38aa3b, v141
	v_exp_f32_e32 v141, v141
	v_cmp_ge_f32_e32 vcc, s7, v139
	s_cmp_eq_u64 vcc, exec
	s_cselect_b64 s[4:5], -1, 0
	s_waitcnt vmcnt(3)
	ds_write_b128 v222, v[114:117] offset:32768
	s_waitcnt lgkmcnt(0)
	s_barrier
	s_waitcnt vmcnt(3)
	v_cndmask_b32_e64 v226, v141, 1.0, s[4:5]
	v_cmp_gt_f32_e32 vcc, 1.0, v226
	s_waitcnt vmcnt(3)
	ds_write_b128 v215, v[118:121]
	ds_write_b128 v216, v[122:125]
	s_cbranch_vccz .LBB0_416
	s_and_saveexec_b64 s[48:49], s[0:1]
	ds_write_b32 v171, v226 offset:128
	s_or_b64 exec, exec, s[48:49]
	s_waitcnt lgkmcnt(0)
	ds_read_b128 v[142:145], v207 offset:224
	ds_read_b128 v[146:149], v207 offset:192
	ds_read_b128 v[150:153], v207 offset:160
	ds_read_b128 v[228:231], v207 offset:128
	s_waitcnt lgkmcnt(3)
	v_pk_mul_f32 v[16:17], v[16:17], v[144:145]
	s_waitcnt lgkmcnt(2)
	v_pk_mul_f32 v[12:13], v[12:13], v[148:149]
	s_waitcnt lgkmcnt(1)
	v_pk_mul_f32 v[8:9], v[8:9], v[152:153]
	s_waitcnt lgkmcnt(0)
	v_pk_mul_f32 v[4:5], v[4:5], v[230:231]
	v_pk_mul_f32 v[14:15], v[14:15], v[142:143]
	v_pk_mul_f32 v[10:11], v[10:11], v[146:147]
	v_pk_mul_f32 v[6:7], v[6:7], v[150:151]
	v_pk_mul_f32 v[2:3], v[2:3], v[228:229]
	v_pk_mul_f32 v[64:65], v[64:65], v[144:145]
	v_pk_mul_f32 v[60:61], v[60:61], v[148:149]
	v_pk_mul_f32 v[56:57], v[56:57], v[152:153]
	v_pk_mul_f32 v[52:53], v[52:53], v[230:231]
	v_pk_mul_f32 v[62:63], v[62:63], v[142:143]
	v_pk_mul_f32 v[58:59], v[58:59], v[146:147]
	v_pk_mul_f32 v[54:55], v[54:55], v[150:151]
	v_pk_mul_f32 v[50:51], v[50:51], v[228:229]
	v_pk_mul_f32 v[48:49], v[48:49], v[144:145]
	v_pk_mul_f32 v[44:45], v[44:45], v[148:149]
	v_pk_mul_f32 v[40:41], v[40:41], v[152:153]
	v_pk_mul_f32 v[36:37], v[36:37], v[230:231]
	v_pk_mul_f32 v[46:47], v[46:47], v[142:143]
	v_pk_mul_f32 v[42:43], v[42:43], v[146:147]
	v_pk_mul_f32 v[38:39], v[38:39], v[150:151]
	v_pk_mul_f32 v[34:35], v[34:35], v[228:229]
	v_pk_mul_f32 v[32:33], v[32:33], v[144:145]
	v_pk_mul_f32 v[28:29], v[28:29], v[148:149]
	v_pk_mul_f32 v[24:25], v[24:25], v[152:153]
	v_pk_mul_f32 v[20:21], v[20:21], v[230:231]
	v_pk_mul_f32 v[30:31], v[30:31], v[142:143]
	v_pk_mul_f32 v[26:27], v[26:27], v[146:147]
	v_pk_mul_f32 v[22:23], v[22:23], v[150:151]
	v_pk_mul_f32 v[18:19], v[18:19], v[228:229]
.LBB0_416:
	v_cndmask_b32_e64 v227, v138, v140, s[4:5]
	v_mul_f32_e32 v228, 0xbe38aa3b, v227
	v_fmamk_f32 v82, v82, 0x3e38aa3b, v228
	v_fmamk_f32 v83, v83, 0x3e38aa3b, v228
	v_fmamk_f32 v84, v84, 0x3e38aa3b, v228
	v_fmamk_f32 v85, v85, 0x3e38aa3b, v228
	v_fmamk_f32 v86, v86, 0x3e38aa3b, v228
	v_fmamk_f32 v87, v87, 0x3e38aa3b, v228
	v_fmamk_f32 v88, v88, 0x3e38aa3b, v228
	v_fmamk_f32 v89, v89, 0x3e38aa3b, v228
	v_fmamk_f32 v90, v90, 0x3e38aa3b, v228
	v_fmamk_f32 v91, v91, 0x3e38aa3b, v228
	v_fmamk_f32 v92, v92, 0x3e38aa3b, v228
	v_fmamk_f32 v93, v93, 0x3e38aa3b, v228
	v_fmamk_f32 v94, v94, 0x3e38aa3b, v228
	v_fmamk_f32 v95, v95, 0x3e38aa3b, v228
	v_fmamk_f32 v96, v96, 0x3e38aa3b, v228
	v_fmamk_f32 v97, v97, 0x3e38aa3b, v228
	v_exp_f32_e32 v138, v82
	v_exp_f32_e32 v153, v83
	v_exp_f32_e32 v139, v84
	v_exp_f32_e32 v152, v85
	v_exp_f32_e32 v140, v86
	v_exp_f32_e32 v151, v87
	v_exp_f32_e32 v141, v88
	v_exp_f32_e32 v150, v89
	v_exp_f32_e32 v142, v90
	v_exp_f32_e32 v149, v91
	v_exp_f32_e32 v143, v92
	v_exp_f32_e32 v148, v93
	v_exp_f32_e32 v144, v94
	v_exp_f32_e32 v147, v95
	v_exp_f32_e32 v145, v96
	v_exp_f32_e32 v146, v97
	v_fmamk_f32 v237, v66, 0x3e38aa3b, v228
	v_fmamk_f32 v238, v67, 0x3e38aa3b, v228
	v_fmamk_f32 v239, v68, 0x3e38aa3b, v228
	v_fmamk_f32 v240, v69, 0x3e38aa3b, v228
	v_fmamk_f32 v241, v70, 0x3e38aa3b, v228
	v_fmamk_f32 v230, v71, 0x3e38aa3b, v228
	v_fmamk_f32 v231, v72, 0x3e38aa3b, v228
	v_fmamk_f32 v232, v73, 0x3e38aa3b, v228
	v_fmamk_f32 v233, v74, 0x3e38aa3b, v228
	v_fmamk_f32 v234, v75, 0x3e38aa3b, v228
	v_fmamk_f32 v235, v76, 0x3e38aa3b, v228
	v_fmamk_f32 v236, v77, 0x3e38aa3b, v228
	v_fmamk_f32 v229, v78, 0x3e38aa3b, v228
	v_fmamk_f32 v242, v79, 0x3e38aa3b, v228
	v_fmamk_f32 v243, v80, 0x3e38aa3b, v228
	v_fmac_f32_e32 v228, 0x3e38aa3b, v81
	s_waitcnt lgkmcnt(0)
; #define LAS __attribute__((address_space(3)))
; #define SBAR() __builtin_amdgcn_sched_barrier(0)
; __device__ __forceinline__ void finishSM(f32x16& p0, f32x16& p1, float alpha, float& l_reg, bf16x8& pa0, bf16x8& pa1, bf16x8& pa2, bf16x8& pa3) {
; #pragma unroll
;     for (int r = 0; r < 16; ++r) p1[r] = __builtin_amdgcn_exp2f(p1[r]);
;     float ps = 0;
; #pragma unroll
;     for (int r = 0; r < 16; ++r) ps += p0[r];
; #pragma unroll
;     for (int r = 0; r < 16; ++r) ps += p1[r];
;     { auto rr = __builtin_amdgcn_permlane32_swap(__float_as_uint(ps), __float_as_uint(ps), false, false);
;       ps = __uint_as_float(rr[0]) + __uint_as_float(rr[1]); }
;     l_reg = l_reg * alpha + ps;
;     ...
;     PK4(p0, 0, pa0); PK4(p0, 8, pa1); PK4(p1, 0, pa2); PK4(p1, 8, pa3);
;     ...
; }
; template <int MODE>
; __device__ __forceinline__ void qkt(f32x16& p0, f32x16& p1, const LAS unsigned char* Ks, const bf16x8* qr, const LAS unsigned char* Qs, int r32, int hi, int cbase) {
;     p0 = f32x16{}; p1 = f32x16{};
; #pragma unroll
;     for (int d0 = 0; d0 < Cfg<MODE>::ND; ++d0) { const int cb = cbase + (d0 * 16 + hi * 8) * 2;
;         const bf16x8 b0 = *(const LAS bf16x8*)(Ks + KSWZ(r32, cb));
;         const bf16x8 b1 = *(const LAS bf16x8*)(Ks + KSWZ(32 + r32, cb));
;         bf16x8 q; if constexpr (MODE == 0) q = *(const LAS bf16x8*)(Qs + KSWZ(r32, cb)); else q = qr[d0];
;         p0 = __builtin_amdgcn_mfma_f32_32x32x16_bf16(b0, q, p0, 0, 0, 0);
;         p1 = __builtin_amdgcn_mfma_f32_32x32x16_bf16(b1, q, p1, 0, 0, 0); }
; template <int MODE>
; __device__ __forceinline__ void attn_pass(const bf16_t* __restrict__ Qb, const bf16_t* __restrict__ Kh, const bf16_t* __restrict__ Vh, const int NT, const int kr0, const int g4, const int map,
;                                           LAS unsigned char* lds, f32x16 (&o)[4]) {
;     ...
;         SBAR(); qkt<MODE>(pA0, pA1, K_lds, qr, Qs, r32, hi, cbase); MASK(pA0, pA1, j + 1);
;         finishSM(pB0, pB1, alB, l_reg, pa0, pa1, pa2, pa3); SBAR();
;         if (j + 3 < NT) SLOAD(SE, j + 3); SBAR();
;         pv_d0(o, vb0 + SHM_V, pa0, pa1, pa2, pa3); partialSM<MODE>(pA0, pA1, m_reg, mnA, alA);
	ds_read_b128 v[66:69], v204 offset:32768
	ds_read_b128 v[70:73], v204 offset:40960
	ds_read_b128 v[244:247], v195 offset:32768
	ds_read_b128 v[248:251], v195 offset:40960
	v_exp_f32_e32 v237, v237
	v_exp_f32_e32 v238, v238
	s_waitcnt lgkmcnt(3)
	v_mfma_f32_32x32x16_bf16 v[82:97], v[66:69], v[110:113], 0
	v_exp_f32_e32 v239, v239
	v_exp_f32_e32 v240, v240
	v_exp_f32_e32 v241, v241
	v_exp_f32_e32 v230, v230
	v_exp_f32_e32 v231, v231
	v_exp_f32_e32 v232, v232
	v_exp_f32_e32 v233, v233
	s_waitcnt lgkmcnt(2)
	v_mfma_f32_32x32x16_bf16 v[66:81], v[70:73], v[110:113], 0
	v_exp_f32_e32 v234, v234
	v_exp_f32_e32 v235, v235
	v_exp_f32_e32 v236, v236
	v_exp_f32_e32 v242, v242
	v_exp_f32_e32 v243, v243
	s_waitcnt lgkmcnt(1)
	v_mfma_f32_32x32x16_bf16 v[82:97], v[244:247], v[106:109], v[82:97]
	s_waitcnt lgkmcnt(0)
	v_mfma_f32_32x32x16_bf16 v[66:81], v[248:251], v[106:109], v[66:81]
	ds_read_b128 v[244:247], v205 offset:32768
	ds_read_b128 v[248:251], v205 offset:40960
	s_waitcnt lgkmcnt(1)
	v_mfma_f32_32x32x16_bf16 v[82:97], v[244:247], v[102:105], v[82:97]
	s_waitcnt lgkmcnt(0)
	v_mfma_f32_32x32x16_bf16 v[66:81], v[248:251], v[102:105], v[66:81]
	ds_read_b128 v[244:247], v206 offset:32768
	ds_read_b128 v[248:251], v206 offset:40960
	s_waitcnt lgkmcnt(1)
	v_mfma_f32_32x32x16_bf16 v[82:97], v[244:247], v[98:101], v[82:97]
	v_exp_f32_e32 v245, v228
	v_add_f32_e32 v228, 0, v138
	v_add_f32_e32 v228, v153, v228
	v_add_f32_e32 v228, v139, v228
	v_add_f32_e32 v228, v152, v228
	v_add_f32_e32 v228, v140, v228
	v_add_f32_e32 v228, v151, v228
	v_add_f32_e32 v228, v141, v228
	v_add_f32_e32 v228, v150, v228
	v_add_f32_e32 v228, v142, v228
	v_add_f32_e32 v228, v149, v228
	v_add_f32_e32 v228, v143, v228
	v_add_f32_e32 v228, v148, v228
	v_add_f32_e32 v228, v144, v228
	v_add_f32_e32 v228, v147, v228
	v_add_f32_e32 v228, v145, v228
	v_add_f32_e32 v228, v146, v228
	v_add_f32_e32 v228, v237, v228
	v_add_f32_e32 v228, v238, v228
	v_add_f32_e32 v228, v239, v228
	v_add_f32_e32 v228, v240, v228
	v_add_f32_e32 v228, v241, v228
	v_add_f32_e32 v228, v230, v228
	v_add_f32_e32 v228, v231, v228
	v_add_f32_e32 v228, v232, v228
	v_exp_f32_e32 v244, v229
	v_add_f32_e32 v228, v233, v228
	v_add_f32_e32 v228, v234, v228
	s_waitcnt lgkmcnt(0)
	v_mfma_f32_32x32x16_bf16 v[66:81], v[248:251], v[98:101], v[66:81]
	v_add_f32_e32 v228, v235, v228
	v_add_f32_e32 v228, v236, v228
	v_add_f32_e32 v228, v244, v228
	v_add_f32_e32 v228, v242, v228
	v_add_f32_e32 v228, v243, v228
	v_add_f32_e32 v228, v245, v228
	v_mov_b32_e32 v229, v228
	v_cvt_pk_bf16_f32 v138, v138, v153
	v_cvt_pk_bf16_f32 v139, v139, v152
	v_cvt_pk_bf16_f32 v140, v140, v151
	v_cvt_pk_bf16_f32 v141, v141, v150
	v_cvt_pk_bf16_f32 v142, v142, v149
	v_cvt_pk_bf16_f32 v143, v143, v148
	v_cvt_pk_bf16_f32 v144, v144, v147
	v_cvt_pk_bf16_f32 v145, v145, v146
	v_cvt_pk_bf16_f32 v150, v237, v238
	v_cvt_pk_bf16_f32 v151, v239, v240
	v_cvt_pk_bf16_f32 v152, v241, v230
	v_cvt_pk_bf16_f32 v153, v231, v232
	v_cvt_pk_bf16_f32 v146, v233, v234
	v_cvt_pk_bf16_f32 v147, v235, v236
	v_cvt_pk_bf16_f32 v148, v244, v242
	v_cvt_pk_bf16_f32 v149, v243, v245
	s_nop 1
	v_permlane32_swap_b32_e32 v228, v229
	v_permlane32_swap_b32_e32 v138, v140
	v_permlane32_swap_b32_e32 v139, v141
	v_permlane32_swap_b32_e32 v142, v144
	v_permlane32_swap_b32_e32 v143, v145
	v_permlane32_swap_b32_e32 v150, v152
	v_permlane32_swap_b32_e32 v151, v153
	v_permlane32_swap_b32_e32 v146, v148
	v_permlane32_swap_b32_e32 v147, v149
	s_cmp_gt_u32 s6, 64
	s_cselect_b64 s[48:49], -1, 0
	s_and_b64 vcc, exec, s[48:49]
	s_cbranch_vccnz .LBB0_418
	v_add_co_u32_e32 v114, vcc, 0x39580000, v200
	s_nop 1
	v_addc_co_u32_e32 v115, vcc, 0, v201, vcc
	v_add_co_u32_e32 v116, vcc, 0x39590000, v200
	s_nop 1
	v_addc_co_u32_e32 v117, vcc, 0, v201, vcc
	global_load_dwordx4 v[118:121], v[114:115], off
	global_load_dwordx4 v[122:125], v[116:117], off
	v_add_co_u32_e32 v114, vcc, 0x38480000, v202
	s_nop 1
	v_addc_co_u32_e32 v115, vcc, 0, v203, vcc
	global_load_dwordx4 v[114:117], v[114:115], off
.LBB0_418:
	ds_read_b64_tr_b16 v[200:201], v173 offset:0
	ds_read_b64_tr_b16 v[202:203], v173 offset:0x800
	ds_read_b64_tr_b16 v[230:231], v173 offset:0x1000
	ds_read_b64_tr_b16 v[232:233], v173 offset:0x1800
	ds_read_b64_tr_b16 v[234:235], v173 offset:0x2000
	ds_read_b64_tr_b16 v[236:237], v173 offset:0x2800
	ds_read_b64_tr_b16 v[238:239], v173 offset:0x3000
	ds_read_b64_tr_b16 v[240:241], v173 offset:0x3800
	s_waitcnt lgkmcnt(0)
	s_nop 0
	v_mfma_f32_32x32x16_bf16 v[2:17], v[138:141], v[200:203], v[2:17]
	ds_read_b64_tr_b16 v[200:201], v173 offset:0x200
	ds_read_b64_tr_b16 v[202:203], v173 offset:0xa00
	v_mfma_f32_32x32x16_bf16 v[2:17], v[142:145], v[230:233], v[2:17]
	ds_read_b64_tr_b16 v[230:231], v173 offset:0x1200
	ds_read_b64_tr_b16 v[232:233], v173 offset:0x1a00
	v_mfma_f32_32x32x16_bf16 v[2:17], v[150:153], v[234:237], v[2:17]
	ds_read_b64_tr_b16 v[234:235], v173 offset:0x2200
	ds_read_b64_tr_b16 v[236:237], v173 offset:0x2a00
	ds_read_b64_tr_b16 v[242:243], v173 offset:0x3200
	ds_read_b64_tr_b16 v[244:245], v173 offset:0x3a00
	s_waitcnt lgkmcnt(0)
	v_mfma_f32_32x32x16_bf16 v[2:17], v[146:149], v[238:241], v[2:17]
	v_mfma_f32_32x32x16_bf16 v[50:65], v[138:141], v[200:203], v[50:65]
	ds_read_b64_tr_b16 v[200:201], v173 offset:0x400
	ds_read_b64_tr_b16 v[202:203], v173 offset:0xc00
	v_mfma_f32_32x32x16_bf16 v[50:65], v[142:145], v[230:233], v[50:65]
	ds_read_b64_tr_b16 v[230:231], v173 offset:0x1400
	ds_read_b64_tr_b16 v[232:233], v173 offset:0x1c00
	v_mfma_f32_32x32x16_bf16 v[50:65], v[150:153], v[234:237], v[50:65]
	ds_read_b64_tr_b16 v[234:235], v173 offset:0x2400
	ds_read_b64_tr_b16 v[236:237], v173 offset:0x2c00
	ds_read_b64_tr_b16 v[238:239], v173 offset:0x3400
	ds_read_b64_tr_b16 v[240:241], v173 offset:0x3c00
	s_waitcnt lgkmcnt(0)
; #define SWAIT() do { if constexpr (MODE == 1) asm volatile("s_waitcnt vmcnt(3)" ::: "memory"); else asm volatile("s_waitcnt vmcnt(4)" ::: "memory"); } while (0)
; #define RESC(a) do { if (__any((a) < 1.f)) { if (hi == 0) al_l[r32] = (a); asm volatile("s_waitcnt lgkmcnt(0)" ::: "memory"); \
;     _Pragma("unroll") for (int d = 0; d < 4; ++d) _Pragma("unroll") for (int r = 0; r < 16; ++r) o[d][r] *= al_l[crow(r, hi)]; } } while (0)
; template <int MODE>
; __device__ __forceinline__ void partialSM(f32x16& p0, f32x16& p1, float& m_reg, float& mn, float& alpha) {
;     constexpr float SCALE = Cfg<MODE>::SCALE, C = SCALE * 1.4426950408889634f;
;     float pmax = p0[0];
; #pragma unroll
;     for (int r = 1; r < 16; ++r) pmax = fmaxf(pmax, p0[r]);
; #pragma unroll
;     for (int r = 0; r < 16; ++r) pmax = fmaxf(pmax, p1[r]);
;     { auto rr = __builtin_amdgcn_permlane32_swap(__float_as_uint(pmax), __float_as_uint(pmax), false, false);
;       pmax = fmaxf(__uint_as_float(rr[0]), __uint_as_float(rr[1])); }
;     if (__builtin_expect(__all(pmax - m_reg <= THR / SCALE), 1)) { mn = m_reg; alpha = 1.f; }
;     else { mn = fmaxf(m_reg, pmax); alpha = __builtin_amdgcn_exp2f((m_reg - mn) * C); m_reg = mn; }
;     const float mnC = -mn * C;
; #pragma unroll
;     for (int r = 0; r < 16; ++r) p0[r] = fmaf(p0[r], C, mnC);
; #pragma unroll
;     for (int r = 0; r < 16; ++r) p1[r] = fmaf(p1[r], C, mnC);
; #pragma unroll
;     for (int r = 0; r < 16; ++r) p0[r] = __builtin_amdgcn_exp2f(p0[r]);
; }
; template <int MODE>
; __device__ __forceinline__ void attn_pass(const bf16_t* __restrict__ Qb, const bf16_t* __restrict__ Kh, const bf16_t* __restrict__ Vh, const int NT, const int kr0, const int g4, const int map,
;                                           LAS unsigned char* lds, f32x16 (&o)[4]) {
;     ...
;         pv_d0(o, vb0 + SHM_V, pa0, pa1, pa2, pa3); partialSM<MODE>(pA0, pA1, m_reg, mnA, alA);
;         __syncthreads(); SWAIT(); SWRITE(1, SO);
;         RESC(alA); __syncthreads();
;     }
	v_mfma_f32_32x32x16_bf16 v[50:65], v[146:149], v[242:245], v[50:65]
	v_mfma_f32_32x32x16_bf16 v[34:49], v[138:141], v[200:203], v[34:49]
	ds_read_b64_tr_b16 v[200:201], v173 offset:0x600
	ds_read_b64_tr_b16 v[202:203], v173 offset:0xe00
	v_mfma_f32_32x32x16_bf16 v[34:49], v[142:145], v[230:233], v[34:49]
	ds_read_b64_tr_b16 v[230:231], v173 offset:0x1600
	ds_read_b64_tr_b16 v[232:233], v173 offset:0x1e00
	v_mfma_f32_32x32x16_bf16 v[34:49], v[150:153], v[234:237], v[34:49]
	ds_read_b64_tr_b16 v[234:235], v173 offset:0x2600
	ds_read_b64_tr_b16 v[236:237], v173 offset:0x2e00
	ds_read_b64_tr_b16 v[242:243], v173 offset:0x3600
	ds_read_b64_tr_b16 v[244:245], v173 offset:0x3e00
	s_waitcnt lgkmcnt(0)
	v_mfma_f32_32x32x16_bf16 v[34:49], v[146:149], v[238:241], v[34:49]
	v_mfma_f32_32x32x16_bf16 v[18:33], v[138:141], v[200:203], v[18:33]
	v_max_f32_e32 v238, v83, v83
	v_max_f32_e32 v239, v82, v82
	v_max_f32_e32 v238, v239, v238
	v_max3_f32 v238, v238, v84, v85
	v_max3_f32 v238, v238, v86, v87
	v_max3_f32 v138, v238, v88, v89
	v_max3_f32 v138, v138, v90, v91
	v_max3_f32 v138, v138, v92, v93
	v_mfma_f32_32x32x16_bf16 v[18:33], v[142:145], v[230:233], v[18:33]
	v_max3_f32 v138, v138, v94, v95
	v_max3_f32 v138, v138, v96, v97
	v_max3_f32 v138, v138, v66, v67
	v_max3_f32 v138, v138, v68, v69
	v_max3_f32 v138, v138, v70, v71
	v_max3_f32 v138, v138, v72, v73
	v_max3_f32 v138, v138, v74, v75
	v_max3_f32 v138, v138, v76, v77
	v_mfma_f32_32x32x16_bf16 v[18:33], v[150:153], v[234:237], v[18:33]
	v_max3_f32 v138, v138, v78, v79
	v_max3_f32 v138, v138, v80, v81
	v_mov_b32_e32 v139, v138
	s_nop 1
	v_permlane32_swap_b32_e32 v138, v139
	v_max_f32_e32 v139, v139, v139
	v_max_f32_e32 v138, v138, v138
	v_max_f32_e32 v138, v138, v139
	v_max_f32_e32 v140, v227, v227
	v_sub_f32_e32 v139, v138, v227
	v_max_f32_e32 v138, v140, v138
	v_mfma_f32_32x32x16_bf16 v[18:33], v[146:149], v[242:245], v[18:33]
	v_sub_f32_e32 v140, v227, v138
	v_mul_f32_e32 v140, 0x3e38aa3b, v140
	v_exp_f32_e32 v140, v140
	v_cmp_ge_f32_e32 vcc, s7, v139
	s_cmp_eq_u64 vcc, exec
	s_cselect_b64 s[4:5], -1, 0
	s_waitcnt vmcnt(0)
	ds_write_b128 v222, v[134:137] offset:49152
	s_waitcnt lgkmcnt(0)
	s_barrier
	s_waitcnt vmcnt(3)
	v_cndmask_b32_e64 v141, v140, 1.0, s[4:5]
	v_cmp_gt_f32_e32 vcc, 1.0, v141
	s_waitcnt vmcnt(2)
	ds_write_b128 v215, v[126:129] offset:16384
	s_waitcnt vmcnt(1)
	ds_write_b128 v216, v[130:133] offset:16384
	s_waitcnt vmcnt(0)
	s_cbranch_vccz .LBB0_422
	s_and_saveexec_b64 s[52:53], s[0:1]
	ds_write_b32 v171, v141 offset:128
	s_or_b64 exec, exec, s[52:53]
	s_waitcnt lgkmcnt(0)
	ds_read_b128 v[126:129], v207 offset:224
	ds_read_b128 v[130:133], v207 offset:192
	ds_read_b128 v[134:137], v207 offset:160
	ds_read_b128 v[142:145], v207 offset:128
	s_waitcnt lgkmcnt(3)
	v_pk_mul_f32 v[16:17], v[16:17], v[128:129]
	s_waitcnt lgkmcnt(2)
	v_pk_mul_f32 v[12:13], v[12:13], v[132:133]
	s_waitcnt lgkmcnt(1)
	v_pk_mul_f32 v[8:9], v[8:9], v[136:137]
	s_waitcnt lgkmcnt(0)
	v_pk_mul_f32 v[4:5], v[4:5], v[144:145]
	v_pk_mul_f32 v[14:15], v[14:15], v[126:127]
	v_pk_mul_f32 v[10:11], v[10:11], v[130:131]
	v_pk_mul_f32 v[6:7], v[6:7], v[134:135]
	v_pk_mul_f32 v[2:3], v[2:3], v[142:143]
	v_pk_mul_f32 v[64:65], v[64:65], v[128:129]
	v_pk_mul_f32 v[60:61], v[60:61], v[132:133]
	v_pk_mul_f32 v[56:57], v[56:57], v[136:137]
	v_pk_mul_f32 v[52:53], v[52:53], v[144:145]
	v_pk_mul_f32 v[62:63], v[62:63], v[126:127]
	v_pk_mul_f32 v[58:59], v[58:59], v[130:131]
	v_pk_mul_f32 v[54:55], v[54:55], v[134:135]
	v_pk_mul_f32 v[50:51], v[50:51], v[142:143]
	v_pk_mul_f32 v[48:49], v[48:49], v[128:129]
	v_pk_mul_f32 v[44:45], v[44:45], v[132:133]
	v_pk_mul_f32 v[40:41], v[40:41], v[136:137]
	v_pk_mul_f32 v[36:37], v[36:37], v[144:145]
	v_pk_mul_f32 v[46:47], v[46:47], v[126:127]
	v_pk_mul_f32 v[42:43], v[42:43], v[130:131]
	v_pk_mul_f32 v[38:39], v[38:39], v[134:135]
	v_pk_mul_f32 v[34:35], v[34:35], v[142:143]
	v_pk_mul_f32 v[32:33], v[32:33], v[128:129]
	v_pk_mul_f32 v[28:29], v[28:29], v[132:133]
	v_pk_mul_f32 v[24:25], v[24:25], v[136:137]
	v_pk_mul_f32 v[20:21], v[20:21], v[144:145]
	v_pk_mul_f32 v[30:31], v[30:31], v[126:127]
	v_pk_mul_f32 v[26:27], v[26:27], v[130:131]
	v_pk_mul_f32 v[22:23], v[22:23], v[134:135]
	v_pk_mul_f32 v[18:19], v[18:19], v[142:143]
.LBB0_422:
	v_cndmask_b32_e64 v140, v138, v227, s[4:5]
	v_mul_f32_e32 v134, 0xbe38aa3b, v140
	v_mov_b32_e32 v135, v134
	v_fmamk_f32 v82, v82, 0x3e38aa3b, v134
	v_fmamk_f32 v83, v83, 0x3e38aa3b, v134
	v_fmamk_f32 v84, v84, 0x3e38aa3b, v134
	v_fmamk_f32 v85, v85, 0x3e38aa3b, v134
	v_fmamk_f32 v86, v86, 0x3e38aa3b, v134
	v_fmamk_f32 v87, v87, 0x3e38aa3b, v134
	v_fmamk_f32 v88, v88, 0x3e38aa3b, v134
	v_fmamk_f32 v89, v89, 0x3e38aa3b, v134
	v_fmamk_f32 v90, v90, 0x3e38aa3b, v134
	v_fmamk_f32 v91, v91, 0x3e38aa3b, v134
	v_fmamk_f32 v92, v92, 0x3e38aa3b, v134
	v_fmamk_f32 v93, v93, 0x3e38aa3b, v134
	v_fmamk_f32 v94, v94, 0x3e38aa3b, v134
	v_fmamk_f32 v95, v95, 0x3e38aa3b, v134
	v_fmamk_f32 v96, v96, 0x3e38aa3b, v134
	v_fmac_f32_e32 v135, 0x3e38aa3b, v97
	v_exp_f32_e32 v201, v82
	v_exp_f32_e32 v203, v83
	v_exp_f32_e32 v153, v84
	v_exp_f32_e32 v202, v85
	v_exp_f32_e32 v151, v86
	v_exp_f32_e32 v200, v87
	v_exp_f32_e32 v150, v88
	v_exp_f32_e32 v152, v89
	v_exp_f32_e32 v147, v90
	v_exp_f32_e32 v149, v91
	v_exp_f32_e32 v145, v92
	v_exp_f32_e32 v148, v93
	v_exp_f32_e32 v143, v94
	v_exp_f32_e32 v146, v95
	v_exp_f32_e32 v142, v96
	v_exp_f32_e32 v144, v135
	v_pk_fma_f32 v[132:133], v[66:67], s[44:45], v[134:135] op_sel_hi:[1,0,0]
	v_pk_fma_f32 v[66:67], v[68:69], s[44:45], v[134:135] op_sel_hi:[1,0,0]
	v_add_f32_e32 v68, v224, v225
	v_fmac_f32_e32 v68, v223, v167
	v_add_f32_e32 v167, v228, v229
	v_pk_fma_f32 v[130:131], v[70:71], s[44:45], v[134:135] op_sel_hi:[1,0,0]
	v_pk_fma_f32 v[128:129], v[72:73], s[44:45], v[134:135] op_sel_hi:[1,0,0]
	v_pk_fma_f32 v[126:127], v[74:75], s[44:45], v[134:135] op_sel_hi:[1,0,0]
	v_pk_fma_f32 v[138:139], v[76:77], s[44:45], v[134:135] op_sel_hi:[1,0,0]
	v_pk_fma_f32 v[136:137], v[78:79], s[44:45], v[134:135] op_sel_hi:[1,0,0]
	v_pk_fma_f32 v[134:135], v[80:81], s[44:45], v[134:135] op_sel_hi:[1,0,0]
	v_fmac_f32_e32 v167, v68, v226
	s_add_i32 s6, s6, 2
	v_lshl_add_u64 v[198:199], v[198:199], 0, s[46:47]
	v_lshl_add_u64 v[196:197], v[196:197], 0, s[46:47]
	s_and_b64 vcc, exec, s[48:49]
	s_waitcnt lgkmcnt(0)
	s_cbranch_vccnz .LBB0_424
	v_mov_b32_e32 v223, v141
	s_branch .LBB0_412

; #define LAS __attribute__((address_space(3)))
; __device__ __forceinline__ void finishSM(f32x16& p0, f32x16& p1, float alpha, float& l_reg, bf16x8& pa0, bf16x8& pa1, bf16x8& pa2, bf16x8& pa3) {
; #pragma unroll
;     for (int r = 0; r < 16; ++r) p1[r] = __builtin_amdgcn_exp2f(p1[r]);
;     float ps = 0;
; #pragma unroll
;     for (int r = 0; r < 16; ++r) ps += p0[r];
; #pragma unroll
;     for (int r = 0; r < 16; ++r) ps += p1[r];
;     { auto rr = __builtin_amdgcn_permlane32_swap(__float_as_uint(ps), __float_as_uint(ps), false, false);
;       ps = __uint_as_float(rr[0]) + __uint_as_float(rr[1]); }
;     l_reg = l_reg * alpha + ps;
;     ...
;     PK4(p0, 0, pa0); PK4(p0, 8, pa1); PK4(p1, 0, pa2); PK4(p1, 8, pa3);
;     ...
; }
; template <int MODE>
; __device__ __forceinline__ void qkt(f32x16& p0, f32x16& p1, const LAS unsigned char* Ks, const bf16x8* qr, const LAS unsigned char* Qs, int r32, int hi, int cbase) {
;     p0 = f32x16{}; p1 = f32x16{};
; #pragma unroll
;     for (int d0 = 0; d0 < Cfg<MODE>::ND; ++d0) { const int cb = cbase + (d0 * 16 + hi * 8) * 2;
;         const bf16x8 b0 = *(const LAS bf16x8*)(Ks + KSWZ(r32, cb));
;         const bf16x8 b1 = *(const LAS bf16x8*)(Ks + KSWZ(32 + r32, cb));
;         bf16x8 q; if constexpr (MODE == 0) q = *(const LAS bf16x8*)(Qs + KSWZ(r32, cb)); else q = qr[d0];
;         p0 = __builtin_amdgcn_mfma_f32_32x32x16_bf16(b0, q, p0, 0, 0, 0);
;         p1 = __builtin_amdgcn_mfma_f32_32x32x16_bf16(b1, q, p1, 0, 0, 0); }
; }
; __device__ __forceinline__ int v_st(int k, int c) { const int kk = (k & ~0xC) | ((k & 4) << 1) | ((k & 8) >> 1); return ((kk >> 3) * 4 + (c >> 5)) * 512 + ((kk & 7) * 32 + (c & 31)) * 2; }
; __device__ __forceinline__ int v_rd_base(int lane) { return ((lane & 3) << 3) | (((lane >> 2) & 3) << 6) | (((lane >> 4) & 1) << 5) | (((lane >> 5) & 1) << 8); }
; template <int OFF> __device__ __forceinline__ s16x4 tr_read(int vb) {
;     s16x4 r; asm volatile("ds_read_b64_tr_b16 %0, %1 offset:%2" : "=&v"(r) : "v"(vb), "i"(OFF) : "memory"); return r;
; }
; template <int D0> __device__ __forceinline__ void pv_one(f32x16& od, int vb, bf16x8 pa0, bf16x8 pa1, bf16x8 pa2, bf16x8 pa3) {
;     const s16x4 l0 = tr_read<v_rd_off(D0, 0, 0)>(vb), h0 = tr_read<v_rd_off(D0, 0, 1)>(vb), l1 = tr_read<v_rd_off(D0, 1, 0)>(vb), h1 = tr_read<v_rd_off(D0, 1, 1)>(vb);
.LBB0_431:
	v_add_f32_e32 v181, 0, v167
	ds_read_b128 v[68:71], v182 offset:49152
	ds_read_b128 v[72:75], v182 offset:57344
	ds_read_b128 v[186:189], v184 offset:49152
	ds_read_b128 v[190:193], v184 offset:57344
	ds_read_b128 v[218:221], v183 offset:49152
	ds_read_b128 v[222:225], v183 offset:57344
	v_add_f32_e32 v181, v169, v181
	s_waitcnt lgkmcnt(5)
	v_mfma_f32_32x32x16_bf16 v[82:97], v[68:71], v[110:113], 0
	v_exp_f32_e32 v141, v66
	v_exp_f32_e32 v201, v67
	v_add_f32_e32 v181, v153, v181
	v_add_f32_e32 v181, v168, v181
	v_add_f32_e32 v181, v151, v181
	v_add_f32_e32 v181, v166, v181
	v_add_f32_e32 v181, v150, v181
	s_waitcnt lgkmcnt(4)
	v_mfma_f32_32x32x16_bf16 v[66:81], v[72:75], v[110:113], 0
	v_add_f32_e32 v181, v152, v181
	v_add_f32_e32 v181, v147, v181
	v_add_f32_e32 v181, v149, v181
	v_add_f32_e32 v181, v145, v181
	v_add_f32_e32 v181, v148, v181
	v_exp_f32_e32 v132, v132
	v_add_f32_e32 v181, v143, v181
	s_waitcnt lgkmcnt(3)
	v_mfma_f32_32x32x16_bf16 v[82:97], v[186:189], v[106:109], v[82:97]
	v_exp_f32_e32 v133, v133
	v_add_f32_e32 v181, v146, v181
	v_add_f32_e32 v181, v142, v181
	v_add_f32_e32 v181, v144, v181
	v_exp_f32_e32 v130, v130
	v_add_f32_e32 v181, v132, v181
	v_exp_f32_e32 v131, v131
	s_waitcnt lgkmcnt(2)
	v_mfma_f32_32x32x16_bf16 v[66:81], v[190:193], v[106:109], v[66:81]
	v_add_f32_e32 v181, v133, v181
	v_exp_f32_e32 v128, v128
	v_add_f32_e32 v181, v141, v181
	v_exp_f32_e32 v129, v129
	v_add_f32_e32 v181, v201, v181
	v_exp_f32_e32 v126, v126
	v_add_f32_e32 v181, v130, v181
	s_waitcnt lgkmcnt(1)
	v_mfma_f32_32x32x16_bf16 v[82:97], v[218:221], v[102:105], v[82:97]
	ds_read_b128 v[226:229], v185 offset:49152
	ds_read_b128 v[230:233], v185 offset:57344
	v_exp_f32_e32 v127, v127
	v_add_f32_e32 v181, v131, v181
	v_exp_f32_e32 v138, v138
	v_add_f32_e32 v181, v128, v181
	v_exp_f32_e32 v139, v139
	v_add_f32_e32 v181, v129, v181
	s_waitcnt lgkmcnt(2)
	v_mfma_f32_32x32x16_bf16 v[66:81], v[222:225], v[102:105], v[66:81]
	v_exp_f32_e32 v136, v136
	v_add_f32_e32 v181, v126, v181
	v_exp_f32_e32 v137, v137
	v_add_f32_e32 v181, v127, v181
	v_exp_f32_e32 v134, v134
	v_add_f32_e32 v181, v138, v181
	v_exp_f32_e32 v135, v135
	s_waitcnt lgkmcnt(1)
	v_mfma_f32_32x32x16_bf16 v[82:97], v[226:229], v[98:101], v[82:97]
	v_add_f32_e32 v181, v139, v181
	v_add_f32_e32 v181, v136, v181
	v_add_f32_e32 v181, v137, v181
	v_add_f32_e32 v181, v134, v181
	v_add_f32_e32 v181, v135, v181
	v_mov_b32_e32 v186, v181
	s_nop 1
	v_permlane32_swap_b32_e32 v181, v186
	s_waitcnt lgkmcnt(0)
	v_mfma_f32_32x32x16_bf16 v[66:81], v[230:233], v[98:101], v[66:81]
	v_cvt_pk_bf16_f32 v188, v167, v169
	v_cvt_pk_bf16_f32 v189, v153, v168
	v_cvt_pk_bf16_f32 v190, v151, v166
	v_cvt_pk_bf16_f32 v191, v150, v152
	v_cvt_pk_bf16_f32 v150, v147, v149
	v_cvt_pk_bf16_f32 v151, v145, v148
	v_cvt_pk_bf16_f32 v152, v143, v146
	v_cvt_pk_bf16_f32 v153, v142, v144
	v_cvt_pk_bf16_f32 v142, v132, v133
	v_cvt_pk_bf16_f32 v143, v141, v201
	v_cvt_pk_bf16_f32 v144, v130, v131
	v_cvt_pk_bf16_f32 v145, v128, v129
	v_cvt_pk_bf16_f32 v146, v126, v127
	v_cvt_pk_bf16_f32 v147, v138, v139
	v_cvt_pk_bf16_f32 v148, v136, v137
	v_cvt_pk_bf16_f32 v149, v134, v135
	s_nop 0
	v_permlane32_swap_b32_e32 v188, v190
	v_permlane32_swap_b32_e32 v189, v191
	v_permlane32_swap_b32_e32 v150, v152
	v_permlane32_swap_b32_e32 v151, v153
	v_permlane32_swap_b32_e32 v142, v144
	v_permlane32_swap_b32_e32 v143, v145
	v_permlane32_swap_b32_e32 v146, v148
	v_permlane32_swap_b32_e32 v147, v149
	v_lshl_add_u64 v[166:167], v[164:165], 0, s[20:21]
	v_add_co_u32_e32 v126, vcc, s43, v166
	v_lshl_add_u64 v[168:169], v[162:163], 0, s[20:21]
	s_nop 0
	v_addc_co_u32_e32 v127, vcc, 0, v167, vcc
	v_add_co_u32_e32 v130, vcc, s45, v166
	s_nop 1
	v_addc_co_u32_e32 v131, vcc, 0, v167, vcc
	v_add_co_u32_e32 v134, vcc, s57, v168
	global_load_dwordx4 v[126:129], v[126:127], off
	s_nop 0
	global_load_dwordx4 v[130:133], v[130:131], off
	v_addc_co_u32_e32 v135, vcc, 0, v169, vcc
	global_load_dwordx4 v[134:137], v[134:135], off offset:128
	ds_read_b64_tr_b16 v[218:219], v175 offset:0
	ds_read_b64_tr_b16 v[220:221], v175 offset:0x800
	ds_read_b64_tr_b16 v[222:223], v175 offset:0x1000
	ds_read_b64_tr_b16 v[224:225], v175 offset:0x1800
	ds_read_b64_tr_b16 v[226:227], v175 offset:0x2000
	ds_read_b64_tr_b16 v[228:229], v175 offset:0x2800
	ds_read_b64_tr_b16 v[230:231], v175 offset:0x3000
	ds_read_b64_tr_b16 v[232:233], v175 offset:0x3800
	s_waitcnt lgkmcnt(0)
	s_nop 0
	v_mfma_f32_32x32x16_bf16 v[2:17], v[188:191], v[218:221], v[2:17]
	ds_read_b64_tr_b16 v[218:219], v175 offset:0x200
	ds_read_b64_tr_b16 v[220:221], v175 offset:0xa00
	v_mfma_f32_32x32x16_bf16 v[2:17], v[150:153], v[222:225], v[2:17]
	ds_read_b64_tr_b16 v[222:223], v175 offset:0x1200
	ds_read_b64_tr_b16 v[224:225], v175 offset:0x1a00
	v_mfma_f32_32x32x16_bf16 v[2:17], v[142:145], v[226:229], v[2:17]
	ds_read_b64_tr_b16 v[226:227], v175 offset:0x2200
	ds_read_b64_tr_b16 v[228:229], v175 offset:0x2a00
	ds_read_b64_tr_b16 v[234:235], v175 offset:0x3200
	ds_read_b64_tr_b16 v[236:237], v175 offset:0x3a00
	s_waitcnt lgkmcnt(0)
	v_mfma_f32_32x32x16_bf16 v[2:17], v[146:149], v[230:233], v[2:17]
	v_mfma_f32_32x32x16_bf16 v[50:65], v[188:191], v[218:221], v[50:65]
	ds_read_b64_tr_b16 v[218:219], v175 offset:0x400
	ds_read_b64_tr_b16 v[220:221], v175 offset:0xc00
	v_mfma_f32_32x32x16_bf16 v[50:65], v[150:153], v[222:225], v[50:65]
	ds_read_b64_tr_b16 v[222:223], v175 offset:0x1400
	ds_read_b64_tr_b16 v[224:225], v175 offset:0x1c00
	v_mfma_f32_32x32x16_bf16 v[50:65], v[142:145], v[226:229], v[50:65]
	ds_read_b64_tr_b16 v[226:227], v175 offset:0x2400
	ds_read_b64_tr_b16 v[228:229], v175 offset:0x2c00
	ds_read_b64_tr_b16 v[230:231], v175 offset:0x3400
	ds_read_b64_tr_b16 v[232:233], v175 offset:0x3c00
	s_waitcnt lgkmcnt(0)
; #define SWAIT() do { if constexpr (MODE == 1) asm volatile("s_waitcnt vmcnt(3)" ::: "memory"); else asm volatile("s_waitcnt vmcnt(4)" ::: "memory"); } while (0)
; #define RESC(a) do { if (__any((a) < 1.f)) { if (hi == 0) al_l[r32] = (a); asm volatile("s_waitcnt lgkmcnt(0)" ::: "memory"); \
;     _Pragma("unroll") for (int d = 0; d < 4; ++d) _Pragma("unroll") for (int r = 0; r < 16; ++r) o[d][r] *= al_l[crow(r, hi)]; } } while (0)
; template <int MODE>
; __device__ __forceinline__ void partialSM(f32x16& p0, f32x16& p1, float& m_reg, float& mn, float& alpha) {
;     constexpr float SCALE = Cfg<MODE>::SCALE, C = SCALE * 1.4426950408889634f;
;     float pmax = p0[0];
; #pragma unroll
;     for (int r = 1; r < 16; ++r) pmax = fmaxf(pmax, p0[r]);
; #pragma unroll
;     for (int r = 0; r < 16; ++r) pmax = fmaxf(pmax, p1[r]);
;     { auto rr = __builtin_amdgcn_permlane32_swap(__float_as_uint(pmax), __float_as_uint(pmax), false, false);
;       pmax = fmaxf(__uint_as_float(rr[0]), __uint_as_float(rr[1])); }
;     if (__builtin_expect(__all(pmax - m_reg <= THR / SCALE), 1)) { mn = m_reg; alpha = 1.f; }
;     else { mn = fmaxf(m_reg, pmax); alpha = __builtin_amdgcn_exp2f((m_reg - mn) * C); m_reg = mn; }
; template <int MODE>
; __device__ __forceinline__ void attn_pass(const bf16_t* __restrict__ Qb, const bf16_t* __restrict__ Kh, const bf16_t* __restrict__ Vh, const int NT, const int kr0, const int g4, const int map,
;                                           LAS unsigned char* lds, f32x16 (&o)[4]) {
;     ...
;         pv_d0(o, vb0, pa0, pa1, pa2, pa3); partialSM<MODE>(pB0, pB1, m_reg, mnB, alB);
;         __syncthreads(); SWAIT(); SWRITE(0, SE);
;         RESC(alB); __syncthreads();
	v_mfma_f32_32x32x16_bf16 v[50:65], v[146:149], v[234:237], v[50:65]
	v_mfma_f32_32x32x16_bf16 v[34:49], v[188:191], v[218:221], v[34:49]
	ds_read_b64_tr_b16 v[218:219], v175 offset:0x600
	ds_read_b64_tr_b16 v[220:221], v175 offset:0xe00
	v_mfma_f32_32x32x16_bf16 v[34:49], v[150:153], v[222:225], v[34:49]
	ds_read_b64_tr_b16 v[222:223], v175 offset:0x1600
	ds_read_b64_tr_b16 v[224:225], v175 offset:0x1e00
	v_mfma_f32_32x32x16_bf16 v[34:49], v[142:145], v[226:229], v[34:49]
	ds_read_b64_tr_b16 v[226:227], v175 offset:0x2600
	ds_read_b64_tr_b16 v[228:229], v175 offset:0x2e00
	ds_read_b64_tr_b16 v[234:235], v175 offset:0x3600
	ds_read_b64_tr_b16 v[236:237], v175 offset:0x3e00
	s_waitcnt lgkmcnt(0)
	v_mfma_f32_32x32x16_bf16 v[34:49], v[146:149], v[230:233], v[34:49]
	v_mfma_f32_32x32x16_bf16 v[18:33], v[188:191], v[218:221], v[18:33]
	v_max_f32_e32 v138, v83, v83
	v_max_f32_e32 v139, v82, v82
	v_max_f32_e32 v138, v139, v138
	v_max3_f32 v138, v138, v84, v85
	v_max3_f32 v138, v138, v86, v87
	v_max3_f32 v138, v138, v88, v89
	v_max3_f32 v138, v138, v90, v91
	v_max3_f32 v138, v138, v92, v93
	v_mfma_f32_32x32x16_bf16 v[18:33], v[150:153], v[222:225], v[18:33]
	v_max3_f32 v138, v138, v94, v95
	v_max3_f32 v138, v138, v96, v97
	v_max3_f32 v138, v138, v66, v67
	v_max3_f32 v138, v138, v68, v69
	v_max3_f32 v138, v138, v70, v71
	v_max3_f32 v138, v138, v72, v73
	v_max3_f32 v138, v138, v74, v75
	v_max3_f32 v138, v138, v76, v77
	v_mfma_f32_32x32x16_bf16 v[18:33], v[142:145], v[226:229], v[18:33]
	v_max3_f32 v138, v138, v78, v79
	v_max3_f32 v138, v138, v80, v81
	v_mov_b32_e32 v139, v138
	s_nop 1
	v_permlane32_swap_b32_e32 v138, v139
	v_max_f32_e32 v139, v139, v139
	v_max_f32_e32 v138, v138, v138
	v_max_f32_e32 v138, v138, v139
	v_max_f32_e32 v141, v140, v140
	v_sub_f32_e32 v139, v138, v140
	v_max_f32_e32 v138, v141, v138
	v_mfma_f32_32x32x16_bf16 v[18:33], v[146:149], v[234:237], v[18:33]
	v_sub_f32_e32 v141, v140, v138
	v_mul_f32_e32 v141, 0x3e38aa3b, v141
	v_exp_f32_e32 v141, v141
	v_cmp_ge_f32_e32 vcc, s7, v139
	s_cmp_eq_u64 vcc, exec
	s_cselect_b64 s[4:5], -1, 0
	s_waitcnt vmcnt(3)
	ds_write_b128 v179, v[122:125] offset:32768
	s_waitcnt lgkmcnt(0)
	s_barrier
	s_waitcnt vmcnt(3)
	v_cndmask_b32_e64 v187, v141, 1.0, s[4:5]
	v_cmp_gt_f32_e32 vcc, 1.0, v187
	s_waitcnt vmcnt(3)
	ds_write_b128 v215, v[114:117]
	ds_write_b128 v216, v[118:121]
	s_cbranch_vccz .LBB0_435
	s_and_saveexec_b64 s[48:49], s[0:1]
	ds_write_b32 v171, v187 offset:128
	s_or_b64 exec, exec, s[48:49]
	s_waitcnt lgkmcnt(0)
	ds_read_b128 v[142:145], v207 offset:224
	ds_read_b128 v[146:149], v207 offset:192
	ds_read_b128 v[150:153], v207 offset:160
	ds_read_b128 v[188:191], v207 offset:128
	s_waitcnt lgkmcnt(3)
	v_pk_mul_f32 v[16:17], v[16:17], v[144:145]
	s_waitcnt lgkmcnt(2)
	v_pk_mul_f32 v[12:13], v[12:13], v[148:149]
	s_waitcnt lgkmcnt(1)
	v_pk_mul_f32 v[8:9], v[8:9], v[152:153]
	s_waitcnt lgkmcnt(0)
	v_pk_mul_f32 v[4:5], v[4:5], v[190:191]
	v_pk_mul_f32 v[14:15], v[14:15], v[142:143]
	v_pk_mul_f32 v[10:11], v[10:11], v[146:147]
	v_pk_mul_f32 v[6:7], v[6:7], v[150:151]
	v_pk_mul_f32 v[2:3], v[2:3], v[188:189]
	v_pk_mul_f32 v[64:65], v[64:65], v[144:145]
	v_pk_mul_f32 v[60:61], v[60:61], v[148:149]
	v_pk_mul_f32 v[56:57], v[56:57], v[152:153]
	v_pk_mul_f32 v[52:53], v[52:53], v[190:191]
	v_pk_mul_f32 v[62:63], v[62:63], v[142:143]
	v_pk_mul_f32 v[58:59], v[58:59], v[146:147]
	v_pk_mul_f32 v[54:55], v[54:55], v[150:151]
	v_pk_mul_f32 v[50:51], v[50:51], v[188:189]
	v_pk_mul_f32 v[48:49], v[48:49], v[144:145]
	v_pk_mul_f32 v[44:45], v[44:45], v[148:149]
	v_pk_mul_f32 v[40:41], v[40:41], v[152:153]
	v_pk_mul_f32 v[36:37], v[36:37], v[190:191]
	v_pk_mul_f32 v[46:47], v[46:47], v[142:143]
	v_pk_mul_f32 v[42:43], v[42:43], v[146:147]
	v_pk_mul_f32 v[38:39], v[38:39], v[150:151]
	v_pk_mul_f32 v[34:35], v[34:35], v[188:189]
	v_pk_mul_f32 v[32:33], v[32:33], v[144:145]
	v_pk_mul_f32 v[28:29], v[28:29], v[148:149]
	v_pk_mul_f32 v[24:25], v[24:25], v[152:153]
	v_pk_mul_f32 v[20:21], v[20:21], v[190:191]
	v_pk_mul_f32 v[30:31], v[30:31], v[142:143]
	v_pk_mul_f32 v[26:27], v[26:27], v[146:147]
	v_pk_mul_f32 v[22:23], v[22:23], v[150:151]
	v_pk_mul_f32 v[18:19], v[18:19], v[188:189]
.LBB0_435:
	v_cndmask_b32_e64 v188, v138, v140, s[4:5]
	v_mul_f32_e32 v189, 0xbe38aa3b, v188
	v_fmamk_f32 v82, v82, 0x3e38aa3b, v189
	v_fmamk_f32 v83, v83, 0x3e38aa3b, v189
	v_fmamk_f32 v84, v84, 0x3e38aa3b, v189
	v_fmamk_f32 v85, v85, 0x3e38aa3b, v189
	v_fmamk_f32 v86, v86, 0x3e38aa3b, v189
	v_fmamk_f32 v87, v87, 0x3e38aa3b, v189
	v_fmamk_f32 v88, v88, 0x3e38aa3b, v189
	v_fmamk_f32 v89, v89, 0x3e38aa3b, v189
	v_fmamk_f32 v90, v90, 0x3e38aa3b, v189
	v_fmamk_f32 v91, v91, 0x3e38aa3b, v189
	v_fmamk_f32 v92, v92, 0x3e38aa3b, v189
	v_fmamk_f32 v93, v93, 0x3e38aa3b, v189
	v_fmamk_f32 v94, v94, 0x3e38aa3b, v189
	v_fmamk_f32 v95, v95, 0x3e38aa3b, v189
	v_fmamk_f32 v96, v96, 0x3e38aa3b, v189
	v_fmamk_f32 v97, v97, 0x3e38aa3b, v189
	v_exp_f32_e32 v138, v82
	v_exp_f32_e32 v153, v83
	v_exp_f32_e32 v139, v84
	v_exp_f32_e32 v152, v85
	v_exp_f32_e32 v140, v86
	v_exp_f32_e32 v151, v87
	v_exp_f32_e32 v141, v88
	v_exp_f32_e32 v150, v89
	v_exp_f32_e32 v142, v90
	v_exp_f32_e32 v149, v91
	v_exp_f32_e32 v143, v92
	v_exp_f32_e32 v148, v93
	v_exp_f32_e32 v144, v94
	v_exp_f32_e32 v147, v95
	v_exp_f32_e32 v145, v96
	v_exp_f32_e32 v146, v97
	v_fmamk_f32 v66, v66, 0x3e38aa3b, v189
	v_fmamk_f32 v67, v67, 0x3e38aa3b, v189
	v_fmamk_f32 v68, v68, 0x3e38aa3b, v189
	v_fmamk_f32 v69, v69, 0x3e38aa3b, v189
	v_fmamk_f32 v70, v70, 0x3e38aa3b, v189
	v_fmamk_f32 v191, v71, 0x3e38aa3b, v189
	v_fmamk_f32 v192, v72, 0x3e38aa3b, v189
	v_fmamk_f32 v193, v73, 0x3e38aa3b, v189
	v_fmamk_f32 v201, v74, 0x3e38aa3b, v189
	v_fmamk_f32 v202, v75, 0x3e38aa3b, v189
	v_fmamk_f32 v203, v76, 0x3e38aa3b, v189
	v_fmamk_f32 v217, v77, 0x3e38aa3b, v189
	v_fmamk_f32 v190, v78, 0x3e38aa3b, v189
	v_fmamk_f32 v218, v79, 0x3e38aa3b, v189
	v_fmamk_f32 v219, v80, 0x3e38aa3b, v189
	v_fmac_f32_e32 v189, 0x3e38aa3b, v81
	s_waitcnt lgkmcnt(0)
; #define LAS __attribute__((address_space(3)))
; #define SBAR() __builtin_amdgcn_sched_barrier(0)
; __device__ __forceinline__ void finishSM(f32x16& p0, f32x16& p1, float alpha, float& l_reg, bf16x8& pa0, bf16x8& pa1, bf16x8& pa2, bf16x8& pa3) {
; #pragma unroll
;     for (int r = 0; r < 16; ++r) p1[r] = __builtin_amdgcn_exp2f(p1[r]);
;     float ps = 0;
; #pragma unroll
;     for (int r = 0; r < 16; ++r) ps += p0[r];
; #pragma unroll
;     for (int r = 0; r < 16; ++r) ps += p1[r];
;     { auto rr = __builtin_amdgcn_permlane32_swap(__float_as_uint(ps), __float_as_uint(ps), false, false);
;       ps = __uint_as_float(rr[0]) + __uint_as_float(rr[1]); }
;     l_reg = l_reg * alpha + ps;
;     ...
;     PK4(p0, 0, pa0); PK4(p0, 8, pa1); PK4(p1, 0, pa2); PK4(p1, 8, pa3);
;     ...
; }
; template <int MODE>
; __device__ __forceinline__ void qkt(f32x16& p0, f32x16& p1, const LAS unsigned char* Ks, const bf16x8* qr, const LAS unsigned char* Qs, int r32, int hi, int cbase) {
;     p0 = f32x16{}; p1 = f32x16{};
; #pragma unroll
;     for (int d0 = 0; d0 < Cfg<MODE>::ND; ++d0) { const int cb = cbase + (d0 * 16 + hi * 8) * 2;
;         const bf16x8 b0 = *(const LAS bf16x8*)(Ks + KSWZ(r32, cb));
;         const bf16x8 b1 = *(const LAS bf16x8*)(Ks + KSWZ(32 + r32, cb));
;         bf16x8 q; if constexpr (MODE == 0) q = *(const LAS bf16x8*)(Qs + KSWZ(r32, cb)); else q = qr[d0];
;         p0 = __builtin_amdgcn_mfma_f32_32x32x16_bf16(b0, q, p0, 0, 0, 0);
;         p1 = __builtin_amdgcn_mfma_f32_32x32x16_bf16(b1, q, p1, 0, 0, 0); }
; template <int MODE>
; __device__ __forceinline__ void attn_pass(const bf16_t* __restrict__ Qb, const bf16_t* __restrict__ Kh, const bf16_t* __restrict__ Vh, const int NT, const int kr0, const int g4, const int map,
;                                           LAS unsigned char* lds, f32x16 (&o)[4]) {
;     ...
;         SBAR(); qkt<MODE>(pA0, pA1, K_lds, qr, Qs, r32, hi, cbase); MASK(pA0, pA1, j + 1);
;         finishSM(pB0, pB1, alB, l_reg, pa0, pa1, pa2, pa3); SBAR();
;         if (j + 3 < NT) SLOAD(SE, j + 3); SBAR();
;         pv_d0(o, vb0 + SHM_V, pa0, pa1, pa2, pa3); partialSM<MODE>(pA0, pA1, m_reg, mnA, alA);
	ds_read_b128 v[72:75], v182 offset:32768
	ds_read_b128 v[76:79], v182 offset:40960
	ds_read_b128 v[220:223], v184 offset:32768
	ds_read_b128 v[224:227], v184 offset:40960
	ds_read_b128 v[228:231], v183 offset:32768
	ds_read_b128 v[232:235], v183 offset:40960
	s_waitcnt lgkmcnt(5)
	v_mfma_f32_32x32x16_bf16 v[82:97], v[72:75], v[110:113], 0
	v_exp_f32_e32 v244, v66
	v_exp_f32_e32 v245, v67
	v_exp_f32_e32 v246, v68
	v_exp_f32_e32 v247, v69
	v_exp_f32_e32 v248, v70
	v_exp_f32_e32 v191, v191
	v_exp_f32_e32 v192, v192
	s_waitcnt lgkmcnt(3)
	v_mfma_f32_32x32x16_bf16 v[82:97], v[220:223], v[106:109], v[82:97]
	v_exp_f32_e32 v221, v189
	v_add_f32_e32 v189, 0, v138
	v_add_f32_e32 v189, v153, v189
	v_add_f32_e32 v189, v139, v189
	v_add_f32_e32 v189, v152, v189
	v_add_f32_e32 v189, v140, v189
	v_add_f32_e32 v189, v151, v189
	v_mfma_f32_32x32x16_bf16 v[66:81], v[76:79], v[110:113], 0
	v_add_f32_e32 v189, v141, v189
	v_add_f32_e32 v189, v150, v189
	v_add_f32_e32 v189, v142, v189
	v_add_f32_e32 v189, v149, v189
	v_add_f32_e32 v189, v143, v189
	v_add_f32_e32 v189, v148, v189
	v_add_f32_e32 v189, v144, v189
	s_waitcnt lgkmcnt(2)
	v_mfma_f32_32x32x16_bf16 v[66:81], v[224:227], v[106:109], v[66:81]
	v_add_f32_e32 v189, v147, v189
	v_add_f32_e32 v189, v145, v189
	v_add_f32_e32 v189, v146, v189
	v_add_f32_e32 v189, v244, v189
	v_add_f32_e32 v189, v245, v189
	v_add_f32_e32 v189, v246, v189
	v_exp_f32_e32 v193, v193
	s_waitcnt lgkmcnt(1)
	v_mfma_f32_32x32x16_bf16 v[82:97], v[228:231], v[102:105], v[82:97]
	v_add_f32_e32 v189, v247, v189
	v_exp_f32_e32 v201, v201
	v_add_f32_e32 v189, v248, v189
	ds_read_b128 v[236:239], v185 offset:32768
	ds_read_b128 v[240:243], v185 offset:40960
	v_exp_f32_e32 v202, v202
	v_add_f32_e32 v189, v191, v189
	v_exp_f32_e32 v203, v203
	s_waitcnt lgkmcnt(2)
	v_mfma_f32_32x32x16_bf16 v[66:81], v[232:235], v[102:105], v[66:81]
	v_add_f32_e32 v189, v192, v189
	v_exp_f32_e32 v217, v217
	v_add_f32_e32 v189, v193, v189
	v_exp_f32_e32 v220, v190
	v_add_f32_e32 v189, v201, v189
	v_exp_f32_e32 v218, v218
	v_add_f32_e32 v189, v202, v189
	v_exp_f32_e32 v219, v219
	s_waitcnt lgkmcnt(1)
	v_mfma_f32_32x32x16_bf16 v[82:97], v[236:239], v[98:101], v[82:97]
	v_add_f32_e32 v189, v203, v189
	v_add_f32_e32 v189, v217, v189
	v_add_f32_e32 v189, v220, v189
	v_add_f32_e32 v189, v218, v189
	v_add_f32_e32 v189, v219, v189
	v_add_f32_e32 v189, v221, v189
	v_mov_b32_e32 v190, v189
	s_waitcnt lgkmcnt(0)
	v_mfma_f32_32x32x16_bf16 v[66:81], v[240:243], v[98:101], v[66:81]
	v_cvt_pk_bf16_f32 v138, v138, v153
	v_cvt_pk_bf16_f32 v139, v139, v152
	v_cvt_pk_bf16_f32 v140, v140, v151
	v_cvt_pk_bf16_f32 v141, v141, v150
	v_cvt_pk_bf16_f32 v142, v142, v149
	v_cvt_pk_bf16_f32 v143, v143, v148
	v_cvt_pk_bf16_f32 v144, v144, v147
	v_cvt_pk_bf16_f32 v145, v145, v146
	v_cvt_pk_bf16_f32 v150, v244, v245
	v_cvt_pk_bf16_f32 v151, v246, v247
	v_cvt_pk_bf16_f32 v152, v248, v191
	v_cvt_pk_bf16_f32 v153, v192, v193
	v_cvt_pk_bf16_f32 v146, v201, v202
	v_cvt_pk_bf16_f32 v147, v203, v217
	v_cvt_pk_bf16_f32 v148, v220, v218
	v_cvt_pk_bf16_f32 v149, v219, v221
	v_permlane32_swap_b32_e32 v189, v190
	v_permlane32_swap_b32_e32 v138, v140
	v_permlane32_swap_b32_e32 v139, v141
	v_permlane32_swap_b32_e32 v142, v144
	v_permlane32_swap_b32_e32 v143, v145
	v_permlane32_swap_b32_e32 v150, v152
	v_permlane32_swap_b32_e32 v151, v153
	v_permlane32_swap_b32_e32 v146, v148
	v_permlane32_swap_b32_e32 v147, v149
	s_cmp_gt_u32 s6, 64
	s_cselect_b64 s[48:49], -1, 0
	s_and_b64 vcc, exec, s[48:49]
	s_cbranch_vccnz .LBB0_437
	v_add_co_u32_e32 v114, vcc, 0x39580000, v166
	s_nop 1
	v_addc_co_u32_e32 v115, vcc, 0, v167, vcc
	v_add_co_u32_e32 v118, vcc, 0x39590000, v166
	s_nop 1
	v_addc_co_u32_e32 v119, vcc, 0, v167, vcc
	v_add_co_u32_e32 v122, vcc, 0x38480000, v168
	global_load_dwordx4 v[114:117], v[114:115], off
	s_nop 0
	global_load_dwordx4 v[118:121], v[118:119], off
	v_addc_co_u32_e32 v123, vcc, 0, v169, vcc
	global_load_dwordx4 v[122:125], v[122:123], off offset:128
.LBB0_437:
	ds_read_b64_tr_b16 v[166:167], v173 offset:0
	ds_read_b64_tr_b16 v[168:169], v173 offset:0x800
	ds_read_b64_tr_b16 v[218:219], v173 offset:0x1000
	ds_read_b64_tr_b16 v[220:221], v173 offset:0x1800
	ds_read_b64_tr_b16 v[222:223], v173 offset:0x2000
	ds_read_b64_tr_b16 v[224:225], v173 offset:0x2800
	ds_read_b64_tr_b16 v[226:227], v173 offset:0x3000
	ds_read_b64_tr_b16 v[228:229], v173 offset:0x3800
	s_waitcnt lgkmcnt(0)
	s_nop 0
	v_mfma_f32_32x32x16_bf16 v[2:17], v[138:141], v[166:169], v[2:17]
	ds_read_b64_tr_b16 v[166:167], v173 offset:0x200
	ds_read_b64_tr_b16 v[168:169], v173 offset:0xa00
	v_mfma_f32_32x32x16_bf16 v[2:17], v[142:145], v[218:221], v[2:17]
	ds_read_b64_tr_b16 v[218:219], v173 offset:0x1200
	ds_read_b64_tr_b16 v[220:221], v173 offset:0x1a00
	v_mfma_f32_32x32x16_bf16 v[2:17], v[150:153], v[222:225], v[2:17]
	ds_read_b64_tr_b16 v[222:223], v173 offset:0x2200
	ds_read_b64_tr_b16 v[224:225], v173 offset:0x2a00
	ds_read_b64_tr_b16 v[230:231], v173 offset:0x3200
	ds_read_b64_tr_b16 v[232:233], v173 offset:0x3a00
	s_waitcnt lgkmcnt(0)
	v_mfma_f32_32x32x16_bf16 v[2:17], v[146:149], v[226:229], v[2:17]
	v_mfma_f32_32x32x16_bf16 v[50:65], v[138:141], v[166:169], v[50:65]
	ds_read_b64_tr_b16 v[166:167], v173 offset:0x400
	ds_read_b64_tr_b16 v[168:169], v173 offset:0xc00
	v_mfma_f32_32x32x16_bf16 v[50:65], v[142:145], v[218:221], v[50:65]
	ds_read_b64_tr_b16 v[218:219], v173 offset:0x1400
	ds_read_b64_tr_b16 v[220:221], v173 offset:0x1c00
	v_mfma_f32_32x32x16_bf16 v[50:65], v[150:153], v[222:225], v[50:65]
	ds_read_b64_tr_b16 v[222:223], v173 offset:0x2400
	ds_read_b64_tr_b16 v[224:225], v173 offset:0x2c00
	ds_read_b64_tr_b16 v[226:227], v173 offset:0x3400
	ds_read_b64_tr_b16 v[228:229], v173 offset:0x3c00
	s_waitcnt lgkmcnt(0)
; #define SWAIT() do { if constexpr (MODE == 1) asm volatile("s_waitcnt vmcnt(3)" ::: "memory"); else asm volatile("s_waitcnt vmcnt(4)" ::: "memory"); } while (0)
; #define RESC(a) do { if (__any((a) < 1.f)) { if (hi == 0) al_l[r32] = (a); asm volatile("s_waitcnt lgkmcnt(0)" ::: "memory"); \
;     _Pragma("unroll") for (int d = 0; d < 4; ++d) _Pragma("unroll") for (int r = 0; r < 16; ++r) o[d][r] *= al_l[crow(r, hi)]; } } while (0)
; template <int MODE>
; __device__ __forceinline__ void partialSM(f32x16& p0, f32x16& p1, float& m_reg, float& mn, float& alpha) {
;     constexpr float SCALE = Cfg<MODE>::SCALE, C = SCALE * 1.4426950408889634f;
;     float pmax = p0[0];
; #pragma unroll
;     for (int r = 1; r < 16; ++r) pmax = fmaxf(pmax, p0[r]);
; #pragma unroll
;     for (int r = 0; r < 16; ++r) pmax = fmaxf(pmax, p1[r]);
;     { auto rr = __builtin_amdgcn_permlane32_swap(__float_as_uint(pmax), __float_as_uint(pmax), false, false);
;       pmax = fmaxf(__uint_as_float(rr[0]), __uint_as_float(rr[1])); }
;     if (__builtin_expect(__all(pmax - m_reg <= THR / SCALE), 1)) { mn = m_reg; alpha = 1.f; }
;     else { mn = fmaxf(m_reg, pmax); alpha = __builtin_amdgcn_exp2f((m_reg - mn) * C); m_reg = mn; }
;     const float mnC = -mn * C;
; #pragma unroll
;     for (int r = 0; r < 16; ++r) p0[r] = fmaf(p0[r], C, mnC);
; #pragma unroll
;     for (int r = 0; r < 16; ++r) p1[r] = fmaf(p1[r], C, mnC);
; #pragma unroll
;     for (int r = 0; r < 16; ++r) p0[r] = __builtin_amdgcn_exp2f(p0[r]);
; }
; template <int MODE>
; __device__ __forceinline__ void attn_pass(const bf16_t* __restrict__ Qb, const bf16_t* __restrict__ Kh, const bf16_t* __restrict__ Vh, const int NT, const int kr0, const int g4, const int map,
;                                           LAS unsigned char* lds, f32x16 (&o)[4]) {
;     ...
;         pv_d0(o, vb0 + SHM_V, pa0, pa1, pa2, pa3); partialSM<MODE>(pA0, pA1, m_reg, mnA, alA);
;         __syncthreads(); SWAIT(); SWRITE(1, SO);
;         RESC(alA); __syncthreads();
;     }
	v_mfma_f32_32x32x16_bf16 v[50:65], v[146:149], v[230:233], v[50:65]
	v_mfma_f32_32x32x16_bf16 v[34:49], v[138:141], v[166:169], v[34:49]
	ds_read_b64_tr_b16 v[166:167], v173 offset:0x600
	ds_read_b64_tr_b16 v[168:169], v173 offset:0xe00
	v_mfma_f32_32x32x16_bf16 v[34:49], v[142:145], v[218:221], v[34:49]
	ds_read_b64_tr_b16 v[218:219], v173 offset:0x1600
	ds_read_b64_tr_b16 v[220:221], v173 offset:0x1e00
	v_mfma_f32_32x32x16_bf16 v[34:49], v[150:153], v[222:225], v[34:49]
	ds_read_b64_tr_b16 v[222:223], v173 offset:0x2600
	ds_read_b64_tr_b16 v[224:225], v173 offset:0x2e00
	ds_read_b64_tr_b16 v[230:231], v173 offset:0x3600
	ds_read_b64_tr_b16 v[232:233], v173 offset:0x3e00
	s_waitcnt lgkmcnt(0)
	v_mfma_f32_32x32x16_bf16 v[34:49], v[146:149], v[226:229], v[34:49]
	v_mfma_f32_32x32x16_bf16 v[18:33], v[138:141], v[166:169], v[18:33]
	v_max_f32_e32 v191, v83, v83
	v_max_f32_e32 v192, v82, v82
	v_max_f32_e32 v191, v192, v191
	v_max3_f32 v191, v191, v84, v85
	v_max3_f32 v191, v191, v86, v87
	v_max3_f32 v138, v191, v88, v89
	v_max3_f32 v138, v138, v90, v91
	v_max3_f32 v138, v138, v92, v93
	v_mfma_f32_32x32x16_bf16 v[18:33], v[142:145], v[218:221], v[18:33]
	v_max3_f32 v138, v138, v94, v95
	v_max3_f32 v138, v138, v96, v97
	v_max3_f32 v138, v138, v66, v67
	v_max3_f32 v138, v138, v68, v69
	v_max3_f32 v138, v138, v70, v71
	v_max3_f32 v138, v138, v72, v73
	v_max3_f32 v138, v138, v74, v75
	v_max3_f32 v138, v138, v76, v77
	v_mfma_f32_32x32x16_bf16 v[18:33], v[150:153], v[222:225], v[18:33]
	v_max3_f32 v138, v138, v78, v79
	v_max3_f32 v138, v138, v80, v81
	v_mov_b32_e32 v139, v138
	s_nop 1
	v_permlane32_swap_b32_e32 v138, v139
	v_max_f32_e32 v139, v139, v139
	v_max_f32_e32 v138, v138, v138
	v_max_f32_e32 v138, v138, v139
	v_max_f32_e32 v140, v188, v188
	v_sub_f32_e32 v139, v138, v188
	v_max_f32_e32 v138, v140, v138
	v_mfma_f32_32x32x16_bf16 v[18:33], v[146:149], v[230:233], v[18:33]
	v_sub_f32_e32 v140, v188, v138
	v_mul_f32_e32 v140, 0x3e38aa3b, v140
	v_exp_f32_e32 v140, v140
	v_cmp_ge_f32_e32 vcc, s7, v139
	s_cmp_eq_u64 vcc, exec
	s_cselect_b64 s[4:5], -1, 0
	s_waitcnt vmcnt(0)
	ds_write_b128 v179, v[134:137] offset:49152
	s_waitcnt lgkmcnt(0)
	s_barrier
	s_waitcnt vmcnt(3)
	v_cndmask_b32_e64 v141, v140, 1.0, s[4:5]
	v_cmp_gt_f32_e32 vcc, 1.0, v141
	s_waitcnt vmcnt(2)
	ds_write_b128 v215, v[126:129] offset:16384
	s_waitcnt vmcnt(1)
	ds_write_b128 v216, v[130:133] offset:16384
	s_waitcnt vmcnt(0)
	s_cbranch_vccz .LBB0_441
	s_and_saveexec_b64 s[52:53], s[0:1]
	ds_write_b32 v171, v141 offset:128
	s_or_b64 exec, exec, s[52:53]
	s_waitcnt lgkmcnt(0)
	ds_read_b128 v[126:129], v207 offset:224
	ds_read_b128 v[130:133], v207 offset:192
	ds_read_b128 v[134:137], v207 offset:160
	ds_read_b128 v[142:145], v207 offset:128
	s_waitcnt lgkmcnt(3)
	v_pk_mul_f32 v[16:17], v[16:17], v[128:129]
	s_waitcnt lgkmcnt(2)
	v_pk_mul_f32 v[12:13], v[12:13], v[132:133]
	s_waitcnt lgkmcnt(1)
	v_pk_mul_f32 v[8:9], v[8:9], v[136:137]
	s_waitcnt lgkmcnt(0)
	v_pk_mul_f32 v[4:5], v[4:5], v[144:145]
	v_pk_mul_f32 v[14:15], v[14:15], v[126:127]
	v_pk_mul_f32 v[10:11], v[10:11], v[130:131]
	v_pk_mul_f32 v[6:7], v[6:7], v[134:135]
	v_pk_mul_f32 v[2:3], v[2:3], v[142:143]
	v_pk_mul_f32 v[64:65], v[64:65], v[128:129]
	v_pk_mul_f32 v[60:61], v[60:61], v[132:133]
	v_pk_mul_f32 v[56:57], v[56:57], v[136:137]
	v_pk_mul_f32 v[52:53], v[52:53], v[144:145]
	v_pk_mul_f32 v[62:63], v[62:63], v[126:127]
	v_pk_mul_f32 v[58:59], v[58:59], v[130:131]
	v_pk_mul_f32 v[54:55], v[54:55], v[134:135]
	v_pk_mul_f32 v[50:51], v[50:51], v[142:143]
	v_pk_mul_f32 v[48:49], v[48:49], v[128:129]
	v_pk_mul_f32 v[44:45], v[44:45], v[132:133]
	v_pk_mul_f32 v[40:41], v[40:41], v[136:137]
	v_pk_mul_f32 v[36:37], v[36:37], v[144:145]
	v_pk_mul_f32 v[46:47], v[46:47], v[126:127]
	v_pk_mul_f32 v[42:43], v[42:43], v[130:131]
	v_pk_mul_f32 v[38:39], v[38:39], v[134:135]
	v_pk_mul_f32 v[34:35], v[34:35], v[142:143]
	v_pk_mul_f32 v[32:33], v[32:33], v[128:129]
	v_pk_mul_f32 v[28:29], v[28:29], v[132:133]
	v_pk_mul_f32 v[24:25], v[24:25], v[136:137]
	v_pk_mul_f32 v[20:21], v[20:21], v[144:145]
	v_pk_mul_f32 v[30:31], v[30:31], v[126:127]
	v_pk_mul_f32 v[26:27], v[26:27], v[130:131]
	v_pk_mul_f32 v[22:23], v[22:23], v[134:135]
	v_pk_mul_f32 v[18:19], v[18:19], v[142:143]
.LBB0_441:
	v_cndmask_b32_e64 v140, v138, v188, s[4:5]
	v_mul_f32_e32 v134, 0xbe38aa3b, v140
	v_mov_b32_e32 v135, v134
	v_fmamk_f32 v82, v82, 0x3e38aa3b, v134
	v_fmamk_f32 v83, v83, 0x3e38aa3b, v134
	v_fmamk_f32 v84, v84, 0x3e38aa3b, v134
	v_fmamk_f32 v85, v85, 0x3e38aa3b, v134
	v_fmamk_f32 v86, v86, 0x3e38aa3b, v134
	v_fmamk_f32 v87, v87, 0x3e38aa3b, v134
	v_fmamk_f32 v88, v88, 0x3e38aa3b, v134
	v_fmamk_f32 v89, v89, 0x3e38aa3b, v134
	v_fmamk_f32 v90, v90, 0x3e38aa3b, v134
	v_fmamk_f32 v91, v91, 0x3e38aa3b, v134
	v_fmamk_f32 v92, v92, 0x3e38aa3b, v134
	v_fmamk_f32 v93, v93, 0x3e38aa3b, v134
	v_fmamk_f32 v94, v94, 0x3e38aa3b, v134
	v_fmamk_f32 v95, v95, 0x3e38aa3b, v134
	v_fmamk_f32 v96, v96, 0x3e38aa3b, v134
	v_fmac_f32_e32 v135, 0x3e38aa3b, v97
	v_exp_f32_e32 v167, v82
	v_exp_f32_e32 v169, v83
	v_exp_f32_e32 v153, v84
	v_exp_f32_e32 v168, v85
	v_exp_f32_e32 v151, v86
	v_exp_f32_e32 v166, v87
	v_exp_f32_e32 v150, v88
	v_exp_f32_e32 v152, v89
	v_exp_f32_e32 v147, v90
	v_exp_f32_e32 v149, v91
	v_exp_f32_e32 v145, v92
	v_exp_f32_e32 v148, v93
	v_exp_f32_e32 v143, v94
	v_exp_f32_e32 v146, v95
	v_exp_f32_e32 v142, v96
	v_exp_f32_e32 v144, v135
	v_pk_fma_f32 v[132:133], v[66:67], s[44:45], v[134:135] op_sel_hi:[1,0,0]
	v_pk_fma_f32 v[66:67], v[68:69], s[44:45], v[134:135] op_sel_hi:[1,0,0]
	v_add_f32_e32 v68, v181, v186
	v_fmac_f32_e32 v68, v180, v178
	v_add_f32_e32 v178, v189, v190
	v_pk_fma_f32 v[130:131], v[70:71], s[44:45], v[134:135] op_sel_hi:[1,0,0]
	v_pk_fma_f32 v[128:129], v[72:73], s[44:45], v[134:135] op_sel_hi:[1,0,0]
	v_pk_fma_f32 v[126:127], v[74:75], s[44:45], v[134:135] op_sel_hi:[1,0,0]
	v_pk_fma_f32 v[138:139], v[76:77], s[44:45], v[134:135] op_sel_hi:[1,0,0]
	v_pk_fma_f32 v[136:137], v[78:79], s[44:45], v[134:135] op_sel_hi:[1,0,0]
	v_pk_fma_f32 v[134:135], v[80:81], s[44:45], v[134:135] op_sel_hi:[1,0,0]
	v_fmac_f32_e32 v178, v68, v187
	s_add_i32 s6, s6, 2
	v_lshl_add_u64 v[162:163], v[162:163], 0, s[46:47]
	v_lshl_add_u64 v[164:165], v[164:165], 0, s[46:47]
	s_and_b64 vcc, exec, s[48:49]
	s_waitcnt lgkmcnt(0)
	s_cbranch_vccnz .LBB0_443
	v_mov_b32_e32 v180, v141
	s_branch .LBB0_431

; #define SBAR() __builtin_amdgcn_sched_barrier(0)
; #define SWAIT() do { if constexpr (MODE == 1) asm volatile("s_waitcnt vmcnt(3)" ::: "memory"); else asm volatile("s_waitcnt vmcnt(4)" ::: "memory"); } while (0)
; #define MASK(P0, P1, jt) do { if (MODE == 0 && (jt) >= 4) { const int kr_ = kr0 + (jt) - 4; const bool rv_ = (kr_ >= r0w) && (kr_ < r0w + 8); int br_ = kr_ - qR + 7; br_ = br_ < 0 ? 0 : (br_ > 14 ? 14 : br_); \
;     na_mask(P0, P1, rv_, biasL + 64 + br_ * 32 + (4 * hi - qc + 15), 4 * hi - cs); } } while (0)
; __device__ __forceinline__ void finishSM(f32x16& p0, f32x16& p1, float alpha, float& l_reg, bf16x8& pa0, bf16x8& pa1, bf16x8& pa2, bf16x8& pa3) {
; #pragma unroll
;     for (int r = 0; r < 16; ++r) p1[r] = __builtin_amdgcn_exp2f(p1[r]);
;     float ps = 0;
; #pragma unroll
;     for (int r = 0; r < 16; ++r) ps += p0[r];
; #pragma unroll
;     for (int r = 0; r < 16; ++r) ps += p1[r];
;     { auto rr = __builtin_amdgcn_permlane32_swap(__float_as_uint(ps), __float_as_uint(ps), false, false);
;       ps = __uint_as_float(rr[0]) + __uint_as_float(rr[1]); }
;     l_reg = l_reg * alpha + ps;
;     ...
;     PK4(p0, 0, pa0); PK4(p0, 8, pa1); PK4(p1, 0, pa2); PK4(p1, 8, pa3);
;     ...
; }
; template <int MODE>
; __device__ __forceinline__ void attn_pass(const bf16_t* __restrict__ Qb, const bf16_t* __restrict__ Kh, const bf16_t* __restrict__ Vh, const int NT, const int kr0, const int g4, const int map,
;                                           LAS unsigned char* lds, f32x16 (&o)[4]) {
;     ...
;     for (int j = 1; j + 1 < NT; j += 2) {
;         SBAR(); qkt<MODE>(pB0, pB1, K_lds + SHM_K, qr, Qs, r32, hi, cbase); MASK(pB0, pB1, j);
;         finishSM(pA0, pA1, alA, l_reg, pa0, pa1, pa2, pa3); SBAR();
;         SLOAD(SO, j + 2 < NT ? j + 2 : NT - 1); SBAR();
;         pv_d0(o, vb0, pa0, pa1, pa2, pa3); partialSM<MODE>(pB0, pB1, m_reg, mnB, alB);
;         __syncthreads(); SWAIT(); SWRITE(0, SE);
.LBB0_465:
	v_add_f32_e32 v68, 0, v234
	v_add_f32_e32 v68, v236, v68
	v_add_f32_e32 v68, v232, v68
	v_add_f32_e32 v68, v235, v68
	v_add_f32_e32 v68, v230, v68
	v_add_f32_e32 v68, v233, v68
	v_add_f32_e32 v68, v229, v68
	v_add_f32_e32 v68, v231, v68
	v_add_f32_e32 v68, v226, v68
	v_add_f32_e32 v68, v228, v68
	v_add_f32_e32 v68, v168, v68
	v_add_f32_e32 v68, v227, v68
	v_exp_f32_e32 v67, v156
	v_add_f32_e32 v68, v166, v68
	v_exp_f32_e32 v72, v157
	v_add_f32_e32 v68, v169, v68
	v_exp_f32_e32 v75, v154
	v_add_f32_e32 v68, v165, v68
	v_exp_f32_e32 v80, v155
	v_add_f32_e32 v68, v167, v68
	v_exp_f32_e32 v100, v152
	v_add_f32_e32 v68, v67, v68
	v_exp_f32_e32 v101, v153
	v_add_f32_e32 v68, v72, v68
	v_exp_f32_e32 v102, v150
	v_add_f32_e32 v68, v75, v68
	v_exp_f32_e32 v103, v151
	v_add_f32_e32 v68, v80, v68
	v_exp_f32_e32 v104, v148
	v_add_f32_e32 v68, v100, v68
	v_exp_f32_e32 v105, v149
	v_add_f32_e32 v68, v101, v68
	v_exp_f32_e32 v106, v146
	v_add_f32_e32 v68, v102, v68
	v_exp_f32_e32 v107, v147
	v_add_f32_e32 v68, v103, v68
	v_exp_f32_e32 v108, v162
	v_add_f32_e32 v68, v104, v68
	v_exp_f32_e32 v109, v163
	v_add_f32_e32 v68, v105, v68
	v_exp_f32_e32 v110, v160
	v_add_f32_e32 v68, v106, v68
	v_exp_f32_e32 v111, v161
	v_add_f32_e32 v68, v107, v68
	v_add_f32_e32 v68, v108, v68
	v_add_f32_e32 v68, v109, v68
	v_add_f32_e32 v68, v110, v68
	v_add_f32_e32 v113, v111, v68
	v_mov_b32_e32 v224, v113
	s_nop 1
	v_permlane32_swap_b32_e32 v113, v224
	v_cvt_pk_bf16_f32 v68, v234, v236
	v_cvt_pk_bf16_f32 v69, v232, v235
	v_cvt_pk_bf16_f32 v70, v230, v233
	v_cvt_pk_bf16_f32 v71, v229, v231
	v_cvt_pk_bf16_f32 v76, v226, v228
	v_cvt_pk_bf16_f32 v77, v168, v227
	v_cvt_pk_bf16_f32 v78, v166, v169
	v_cvt_pk_bf16_f32 v79, v165, v167
	v_cvt_pk_bf16_f32 v98, v67, v72
	v_cvt_pk_bf16_f32 v99, v75, v80
	v_cvt_pk_bf16_f32 v100, v100, v101
	v_cvt_pk_bf16_f32 v101, v102, v103
	v_cvt_pk_bf16_f32 v102, v104, v105
	v_cvt_pk_bf16_f32 v103, v106, v107
	v_cvt_pk_bf16_f32 v104, v108, v109
	v_cvt_pk_bf16_f32 v105, v110, v111
	s_nop 0
	v_permlane32_swap_b32_e32 v68, v70
	v_permlane32_swap_b32_e32 v69, v71
	v_permlane32_swap_b32_e32 v76, v78
	v_permlane32_swap_b32_e32 v77, v79
	v_permlane32_swap_b32_e32 v98, v100
	v_permlane32_swap_b32_e32 v99, v101
	v_permlane32_swap_b32_e32 v102, v104
	v_permlane32_swap_b32_e32 v103, v105
	s_cmp_gt_u32 s6, 1
	s_cselect_b32 s4, s3, 0x10c0
	s_ashr_i32 s5, s4, 31
	v_mov_b32_e32 v107, s5
	v_or_b32_e32 v106, s4, v174
	v_lshlrev_b64 v[106:107], 11, v[106:107]
	v_lshl_add_u64 v[110:111], v[176:177], 0, s[4:5]
	v_or_b32_e32 v106, v106, v190
	v_lshlrev_b64 v[110:111], 11, v[110:111]
	v_lshl_add_u64 v[108:109], s[38:39], 0, v[106:107]
	v_or_b32_e32 v110, v110, v190
	v_lshl_add_u64 v[106:107], s[24:25], 0, v[106:107]
	v_lshl_add_u64 v[114:115], s[38:39], 0, v[110:111]
	global_load_dwordx4 v[146:149], v[108:109], off
	global_load_dwordx4 v[150:153], v[114:115], off
	v_lshl_add_u64 v[108:109], s[24:25], 0, v[110:111]
	global_load_dwordx4 v[154:157], v[106:107], off
	global_load_dwordx4 v[158:161], v[108:109], off
	ds_read_b64_tr_b16 v[106:107], v175 offset:0
	ds_read_b64_tr_b16 v[108:109], v175 offset:0x800
	ds_read_b64_tr_b16 v[114:115], v175 offset:0x1000
	ds_read_b64_tr_b16 v[116:117], v175 offset:0x1800
	ds_read_b64_tr_b16 v[118:119], v175 offset:0x2000
	ds_read_b64_tr_b16 v[120:121], v175 offset:0x2800
	ds_read_b64_tr_b16 v[122:123], v175 offset:0x3000
	ds_read_b64_tr_b16 v[124:125], v175 offset:0x3800
	s_waitcnt lgkmcnt(0)
	s_nop 0
	v_mfma_f32_32x32x16_bf16 v[2:17], v[68:71], v[106:109], v[2:17]
	ds_read_b64_tr_b16 v[106:107], v175 offset:0x200
	ds_read_b64_tr_b16 v[108:109], v175 offset:0xa00
	v_mfma_f32_32x32x16_bf16 v[2:17], v[76:79], v[114:117], v[2:17]
	ds_read_b64_tr_b16 v[114:115], v175 offset:0x1200
	ds_read_b64_tr_b16 v[116:117], v175 offset:0x1a00
	v_mfma_f32_32x32x16_bf16 v[2:17], v[98:101], v[118:121], v[2:17]
	ds_read_b64_tr_b16 v[118:119], v175 offset:0x2200
	ds_read_b64_tr_b16 v[120:121], v175 offset:0x2a00
	ds_read_b64_tr_b16 v[126:127], v175 offset:0x3200
	ds_read_b64_tr_b16 v[128:129], v175 offset:0x3a00
	s_waitcnt lgkmcnt(0)
	v_mfma_f32_32x32x16_bf16 v[2:17], v[102:105], v[122:125], v[2:17]
	v_mfma_f32_32x32x16_bf16 v[50:65], v[68:71], v[106:109], v[50:65]
	ds_read_b64_tr_b16 v[106:107], v175 offset:0x400
	ds_read_b64_tr_b16 v[108:109], v175 offset:0xc00
	v_mfma_f32_32x32x16_bf16 v[50:65], v[76:79], v[114:117], v[50:65]
	ds_read_b64_tr_b16 v[114:115], v175 offset:0x1400
	ds_read_b64_tr_b16 v[116:117], v175 offset:0x1c00
	v_mfma_f32_32x32x16_bf16 v[50:65], v[98:101], v[118:121], v[50:65]
	ds_read_b64_tr_b16 v[118:119], v175 offset:0x2400
	ds_read_b64_tr_b16 v[120:121], v175 offset:0x2c00
	ds_read_b64_tr_b16 v[122:123], v175 offset:0x3400
	ds_read_b64_tr_b16 v[124:125], v175 offset:0x3c00
	s_waitcnt lgkmcnt(0)
	v_mfma_f32_32x32x16_bf16 v[50:65], v[102:105], v[126:129], v[50:65]
	v_mfma_f32_32x32x16_bf16 v[34:49], v[68:71], v[106:109], v[34:49]
	ds_read_b64_tr_b16 v[106:107], v175 offset:0x600
	ds_read_b64_tr_b16 v[108:109], v175 offset:0xe00
	v_mfma_f32_32x32x16_bf16 v[34:49], v[76:79], v[114:117], v[34:49]
	ds_read_b64_tr_b16 v[114:115], v175 offset:0x1600
	ds_read_b64_tr_b16 v[116:117], v175 offset:0x1e00
	v_mfma_f32_32x32x16_bf16 v[34:49], v[98:101], v[118:121], v[34:49]
	ds_read_b64_tr_b16 v[118:119], v175 offset:0x2600
	ds_read_b64_tr_b16 v[120:121], v175 offset:0x2e00
	ds_read_b64_tr_b16 v[126:127], v175 offset:0x3600
	ds_read_b64_tr_b16 v[128:129], v175 offset:0x3e00
	s_waitcnt lgkmcnt(0)
	v_mfma_f32_32x32x16_bf16 v[34:49], v[102:105], v[122:125], v[34:49]
	v_mfma_f32_32x32x16_bf16 v[18:33], v[68:71], v[106:109], v[18:33]
	v_max_f32_e32 v67, v83, v83
	v_max_f32_e32 v72, v82, v82
	v_max_f32_e32 v67, v72, v67
	v_max3_f32 v67, v67, v84, v85
	v_max3_f32 v67, v67, v86, v87
	v_max3_f32 v67, v67, v88, v89
	v_max3_f32 v67, v67, v90, v91
	v_max3_f32 v67, v67, v92, v93
	v_mfma_f32_32x32x16_bf16 v[18:33], v[76:79], v[114:117], v[18:33]
	v_max3_f32 v67, v67, v94, v95
	v_max3_f32 v67, v67, v96, v97
	v_max3_f32 v67, v67, v66, v237
	v_max3_f32 v67, v67, v238, v239
	v_max3_f32 v67, v67, v240, v241
	v_max3_f32 v67, v67, v242, v73
	v_max3_f32 v67, v67, v74, v243
	v_max3_f32 v67, v67, v244, v245
	v_mfma_f32_32x32x16_bf16 v[18:33], v[98:101], v[118:121], v[18:33]
	v_max3_f32 v67, v67, v246, v247
	v_max3_f32 v67, v67, v250, v81
	v_mov_b32_e32 v68, v67
	s_nop 1
	v_permlane32_swap_b32_e32 v67, v68
	v_max_f32_e32 v68, v68, v68
	v_max_f32_e32 v67, v67, v67
	v_max_f32_e32 v67, v67, v68
	v_max_f32_e32 v69, v164, v164
	v_sub_f32_e32 v68, v67, v164
	v_max_f32_e32 v67, v69, v67
	v_mfma_f32_32x32x16_bf16 v[18:33], v[102:105], v[126:129], v[18:33]
	v_sub_f32_e32 v69, v164, v67
	v_mul_f32_e32 v69, 0x3e0293ee, v69
	v_exp_f32_e32 v69, v69
	v_cmp_ge_f32_e32 vcc, s7, v68
	s_cmp_eq_u64 vcc, exec
	s_cselect_b64 s[4:5], -1, 0
	s_waitcnt vmcnt(4)
	ds_write_b128 v192, v[138:141] offset:32768
	ds_write_b128 v193, v[142:145] offset:32768
	s_waitcnt lgkmcnt(0)
	s_barrier
; #define LAS __attribute__((address_space(3)))
; #define SBAR() __builtin_amdgcn_sched_barrier(0)
; #define SWAIT() do { if constexpr (MODE == 1) asm volatile("s_waitcnt vmcnt(3)" ::: "memory"); else asm volatile("s_waitcnt vmcnt(4)" ::: "memory"); } while (0)
; #define RESC(a) do { if (__any((a) < 1.f)) { if (hi == 0) al_l[r32] = (a); asm volatile("s_waitcnt lgkmcnt(0)" ::: "memory"); \
;     _Pragma("unroll") for (int d = 0; d < 4; ++d) _Pragma("unroll") for (int r = 0; r < 16; ++r) o[d][r] *= al_l[crow(r, hi)]; } } while (0)
; #define MASK(P0, P1, jt) do { if (MODE == 0 && (jt) >= 4) { const int kr_ = kr0 + (jt) - 4; const bool rv_ = (kr_ >= r0w) && (kr_ < r0w + 8); int br_ = kr_ - qR + 7; br_ = br_ < 0 ? 0 : (br_ > 14 ? 14 : br_); \
;     na_mask(P0, P1, rv_, biasL + 64 + br_ * 32 + (4 * hi - qc + 15), 4 * hi - cs); } } while (0)
; template <int MODE>
; __device__ __forceinline__ void qkt(f32x16& p0, f32x16& p1, const LAS unsigned char* Ks, const bf16x8* qr, const LAS unsigned char* Qs, int r32, int hi, int cbase) {
;     p0 = f32x16{}; p1 = f32x16{};
; #pragma unroll
;     for (int d0 = 0; d0 < Cfg<MODE>::ND; ++d0) { const int cb = cbase + (d0 * 16 + hi * 8) * 2;
;         const bf16x8 b0 = *(const LAS bf16x8*)(Ks + KSWZ(r32, cb));
;         const bf16x8 b1 = *(const LAS bf16x8*)(Ks + KSWZ(32 + r32, cb));
;         bf16x8 q; if constexpr (MODE == 0) q = *(const LAS bf16x8*)(Qs + KSWZ(r32, cb)); else q = qr[d0];
;         p0 = __builtin_amdgcn_mfma_f32_32x32x16_bf16(b0, q, p0, 0, 0, 0);
;         p1 = __builtin_amdgcn_mfma_f32_32x32x16_bf16(b1, q, p1, 0, 0, 0); }
; template <int MODE>
; __device__ __forceinline__ void attn_pass(const bf16_t* __restrict__ Qb, const bf16_t* __restrict__ Kh, const bf16_t* __restrict__ Vh, const int NT, const int kr0, const int g4, const int map,
;                                           LAS unsigned char* lds, f32x16 (&o)[4]) {
;     ...
;         __syncthreads(); SWAIT(); SWRITE(0, SE);
;         RESC(alB); __syncthreads();
;         SBAR(); qkt<MODE>(pA0, pA1, K_lds, qr, Qs, r32, hi, cbase); MASK(pA0, pA1, j + 1);
	s_waitcnt vmcnt(4)
	v_cndmask_b32_e64 v225, v69, 1.0, s[4:5]
	v_cmp_gt_f32_e32 vcc, 1.0, v225
	s_waitcnt vmcnt(4)
	ds_write_b128 v199, v[130:133]
	ds_write_b128 v200, v[134:137]
	s_cbranch_vccz .LBB0_469
	s_and_saveexec_b64 s[42:43], s[0:1]
	ds_write_b32 v171, v225 offset:128
	s_or_b64 exec, exec, s[42:43]
	s_waitcnt lgkmcnt(0)
	ds_read_b128 v[68:71], v207 offset:224
	ds_read_b128 v[76:79], v207 offset:192
	ds_read_b128 v[98:101], v207 offset:160
	ds_read_b128 v[102:105], v207 offset:128
	s_waitcnt lgkmcnt(3)
	v_pk_mul_f32 v[16:17], v[16:17], v[70:71]
	s_waitcnt lgkmcnt(2)
	v_pk_mul_f32 v[12:13], v[12:13], v[78:79]
	s_waitcnt lgkmcnt(1)
	v_pk_mul_f32 v[8:9], v[8:9], v[100:101]
	s_waitcnt lgkmcnt(0)
	v_pk_mul_f32 v[4:5], v[4:5], v[104:105]
	v_pk_mul_f32 v[14:15], v[14:15], v[68:69]
	v_pk_mul_f32 v[10:11], v[10:11], v[76:77]
	v_pk_mul_f32 v[6:7], v[6:7], v[98:99]
	v_pk_mul_f32 v[2:3], v[2:3], v[102:103]
	v_pk_mul_f32 v[64:65], v[64:65], v[70:71]
	v_pk_mul_f32 v[60:61], v[60:61], v[78:79]
	v_pk_mul_f32 v[56:57], v[56:57], v[100:101]
	v_pk_mul_f32 v[52:53], v[52:53], v[104:105]
	v_pk_mul_f32 v[62:63], v[62:63], v[68:69]
	v_pk_mul_f32 v[58:59], v[58:59], v[76:77]
	v_pk_mul_f32 v[54:55], v[54:55], v[98:99]
	v_pk_mul_f32 v[50:51], v[50:51], v[102:103]
	v_pk_mul_f32 v[48:49], v[48:49], v[70:71]
	v_pk_mul_f32 v[44:45], v[44:45], v[78:79]
	v_pk_mul_f32 v[40:41], v[40:41], v[100:101]
	v_pk_mul_f32 v[36:37], v[36:37], v[104:105]
	v_pk_mul_f32 v[46:47], v[46:47], v[68:69]
	v_pk_mul_f32 v[42:43], v[42:43], v[76:77]
	v_pk_mul_f32 v[38:39], v[38:39], v[98:99]
	v_pk_mul_f32 v[34:35], v[34:35], v[102:103]
	v_pk_mul_f32 v[32:33], v[32:33], v[70:71]
	v_pk_mul_f32 v[28:29], v[28:29], v[78:79]
	v_pk_mul_f32 v[24:25], v[24:25], v[100:101]
	v_pk_mul_f32 v[20:21], v[20:21], v[104:105]
	v_pk_mul_f32 v[30:31], v[30:31], v[68:69]
	v_pk_mul_f32 v[26:27], v[26:27], v[76:77]
	v_pk_mul_f32 v[22:23], v[22:23], v[98:99]
	v_pk_mul_f32 v[18:19], v[18:19], v[102:103]
.LBB0_469:
	v_cndmask_b32_e64 v226, v67, v164, s[4:5]
	v_mul_f32_e32 v235, 0xbe0293ee, v226
	v_fmamk_f32 v67, v82, 0x3e0293ee, v235
	v_fmamk_f32 v68, v83, 0x3e0293ee, v235
	v_fmamk_f32 v69, v84, 0x3e0293ee, v235
	v_fmamk_f32 v70, v85, 0x3e0293ee, v235
	v_fmamk_f32 v71, v86, 0x3e0293ee, v235
	v_fmamk_f32 v72, v87, 0x3e0293ee, v235
	v_fmamk_f32 v75, v88, 0x3e0293ee, v235
	v_fmamk_f32 v76, v89, 0x3e0293ee, v235
	v_fmamk_f32 v77, v90, 0x3e0293ee, v235
	v_fmamk_f32 v78, v91, 0x3e0293ee, v235
	v_fmamk_f32 v79, v92, 0x3e0293ee, v235
	v_fmamk_f32 v80, v93, 0x3e0293ee, v235
	v_fmamk_f32 v82, v94, 0x3e0293ee, v235
	v_fmamk_f32 v83, v95, 0x3e0293ee, v235
	v_fmamk_f32 v84, v96, 0x3e0293ee, v235
	v_fmamk_f32 v85, v97, 0x3e0293ee, v235
	v_exp_f32_e32 v232, v67
	v_exp_f32_e32 v234, v68
	v_exp_f32_e32 v230, v69
	v_exp_f32_e32 v233, v70
	v_exp_f32_e32 v228, v71
	v_exp_f32_e32 v231, v72
	v_exp_f32_e32 v227, v75
	v_exp_f32_e32 v229, v76
	v_exp_f32_e32 v167, v77
	v_exp_f32_e32 v169, v78
	v_exp_f32_e32 v165, v79
	v_exp_f32_e32 v168, v80
	v_exp_f32_e32 v163, v82
	v_exp_f32_e32 v166, v83
	v_exp_f32_e32 v162, v84
	v_exp_f32_e32 v164, v85
	v_fmamk_f32 v236, v66, 0x3e0293ee, v235
	v_fmamk_f32 v237, v237, 0x3e0293ee, v235
	v_fmamk_f32 v238, v238, 0x3e0293ee, v235
	v_fmamk_f32 v239, v239, 0x3e0293ee, v235
	v_fmamk_f32 v240, v240, 0x3e0293ee, v235
	v_fmamk_f32 v241, v241, 0x3e0293ee, v235
	v_fmamk_f32 v242, v242, 0x3e0293ee, v235
	v_fmamk_f32 v248, v73, 0x3e0293ee, v235
	v_fmamk_f32 v249, v74, 0x3e0293ee, v235
	v_fmamk_f32 v243, v243, 0x3e0293ee, v235
	v_fmamk_f32 v244, v244, 0x3e0293ee, v235
	v_fmamk_f32 v245, v245, 0x3e0293ee, v235
	v_fmamk_f32 v246, v246, 0x3e0293ee, v235
	v_fmamk_f32 v247, v247, 0x3e0293ee, v235
	v_fmamk_f32 v250, v250, 0x3e0293ee, v235
	v_fmac_f32_e32 v235, 0x3e0293ee, v81
	s_waitcnt lgkmcnt(0)
	ds_read_b128 v[66:69], v201 offset:32768
	ds_read_b128 v[70:73], v202
	s_cmp_gt_u32 s6, 2
	s_mov_b64 s[4:5], -1
	s_waitcnt lgkmcnt(0)
	v_mfma_f32_32x32x16_bf16 v[82:97], v[66:69], v[70:73], 0
	ds_read_b128 v[66:69], v204 offset:40960
	ds_read_b128 v[98:101], v195 offset:40960
	ds_read_b128 v[102:105], v203 offset:32768
	ds_read_b128 v[106:109], v209
	s_waitcnt lgkmcnt(3)
	v_mfma_f32_32x32x16_bf16 v[66:81], v[66:69], v[70:73], 0
	s_waitcnt lgkmcnt(0)
	v_mfma_f32_32x32x16_bf16 v[82:97], v[102:105], v[106:109], v[82:97]
	v_mfma_f32_32x32x16_bf16 v[66:81], v[98:101], v[106:109], v[66:81]
	ds_read_b128 v[98:101], v210 offset:32768
	ds_read_b128 v[102:105], v211
	s_waitcnt lgkmcnt(0)
	v_mfma_f32_32x32x16_bf16 v[82:97], v[98:101], v[102:105], v[82:97]
	ds_read_b128 v[98:101], v205 offset:40960
	ds_read_b128 v[106:109], v206 offset:40960
	s_waitcnt lgkmcnt(1)
	v_mfma_f32_32x32x16_bf16 v[66:81], v[98:101], v[102:105], v[66:81]
	ds_read_b128 v[98:101], v212 offset:32768
	ds_read_b128 v[102:105], v213
	s_waitcnt lgkmcnt(0)
	v_mfma_f32_32x32x16_bf16 v[82:97], v[98:101], v[102:105], v[82:97]
	v_mfma_f32_32x32x16_bf16 v[66:81], v[106:109], v[102:105], v[66:81]
	ds_read_b128 v[98:101], v197 offset:32768
	ds_read_b128 v[102:105], v214
	s_waitcnt lgkmcnt(0)
	v_mfma_f32_32x32x16_bf16 v[82:97], v[98:101], v[102:105], v[82:97]
	ds_read_b128 v[98:101], v182 offset:40960
	ds_read_b128 v[106:109], v184 offset:40960
	s_waitcnt lgkmcnt(1)
	v_mfma_f32_32x32x16_bf16 v[66:81], v[98:101], v[102:105], v[66:81]
	ds_read_b128 v[98:101], v198 offset:32768
	ds_read_b128 v[102:105], v215
	s_waitcnt lgkmcnt(0)
	v_mfma_f32_32x32x16_bf16 v[82:97], v[98:101], v[102:105], v[82:97]
	v_mfma_f32_32x32x16_bf16 v[66:81], v[106:109], v[102:105], v[66:81]
	ds_read_b128 v[98:101], v216 offset:32768
	ds_read_b128 v[102:105], v217
	s_waitcnt lgkmcnt(0)
	v_mfma_f32_32x32x16_bf16 v[82:97], v[98:101], v[102:105], v[82:97]
	ds_read_b128 v[98:101], v183 offset:40960
	ds_read_b128 v[106:109], v185 offset:40960
	s_waitcnt lgkmcnt(1)
	v_mfma_f32_32x32x16_bf16 v[66:81], v[98:101], v[102:105], v[66:81]
	ds_read_b128 v[98:101], v194 offset:32768
	ds_read_b128 v[102:105], v218
	s_waitcnt lgkmcnt(0)
	v_mfma_f32_32x32x16_bf16 v[82:97], v[98:101], v[102:105], v[82:97]
	v_mfma_f32_32x32x16_bf16 v[66:81], v[106:109], v[102:105], v[66:81]
	s_cbranch_scc1 .LBB0_471
	s_nop 10
	v_mov_b64_e32 v[128:129], v[80:81]
	s_mov_b64 s[4:5], 0
	v_mov_b32_e32 v112, v80
	v_mov_b32_e32 v111, v79
	v_mov_b32_e32 v110, v78
	v_mov_b32_e32 v109, v77
	v_mov_b32_e32 v108, v76
	v_mov_b32_e32 v107, v75
	v_mov_b32_e32 v104, v72
	v_mov_b32_e32 v103, v71
	v_mov_b32_e32 v102, v70
	v_mov_b32_e32 v101, v69
	v_mov_b32_e32 v100, v68
	v_mov_b32_e32 v99, v67
	v_mov_b64_e32 v[126:127], v[78:79]
	v_mov_b64_e32 v[124:125], v[76:77]
	v_mov_b64_e32 v[122:123], v[74:75]
	v_mov_b64_e32 v[120:121], v[72:73]
	v_mov_b64_e32 v[118:119], v[70:71]
	v_mov_b64_e32 v[116:117], v[68:69]
	v_mov_b64_e32 v[114:115], v[66:67]

; #define SWAIT() do { if constexpr (MODE == 1) asm volatile("s_waitcnt vmcnt(3)" ::: "memory"); else asm volatile("s_waitcnt vmcnt(4)" ::: "memory"); } while (0)
; #define RESC(a) do { if (__any((a) < 1.f)) { if (hi == 0) al_l[r32] = (a); asm volatile("s_waitcnt lgkmcnt(0)" ::: "memory"); \
;     _Pragma("unroll") for (int d = 0; d < 4; ++d) _Pragma("unroll") for (int r = 0; r < 16; ++r) o[d][r] *= al_l[crow(r, hi)]; } } while (0)
; template <int MODE>
; __device__ __forceinline__ void partialSM(f32x16& p0, f32x16& p1, float& m_reg, float& mn, float& alpha) {
;     constexpr float SCALE = Cfg<MODE>::SCALE, C = SCALE * 1.4426950408889634f;
;     float pmax = p0[0];
; #pragma unroll
;     for (int r = 1; r < 16; ++r) pmax = fmaxf(pmax, p0[r]);
; #pragma unroll
;     for (int r = 0; r < 16; ++r) pmax = fmaxf(pmax, p1[r]);
;     { auto rr = __builtin_amdgcn_permlane32_swap(__float_as_uint(pmax), __float_as_uint(pmax), false, false);
;       pmax = fmaxf(__uint_as_float(rr[0]), __uint_as_float(rr[1])); }
;     if (__builtin_expect(__all(pmax - m_reg <= THR / SCALE), 1)) { mn = m_reg; alpha = 1.f; }
;     else { mn = fmaxf(m_reg, pmax); alpha = __builtin_amdgcn_exp2f((m_reg - mn) * C); m_reg = mn; }
;     const float mnC = -mn * C;
; #pragma unroll
;     for (int r = 0; r < 16; ++r) p0[r] = fmaf(p0[r], C, mnC);
; #pragma unroll
;     for (int r = 0; r < 16; ++r) p1[r] = fmaf(p1[r], C, mnC);
; #pragma unroll
;     for (int r = 0; r < 16; ++r) p0[r] = __builtin_amdgcn_exp2f(p0[r]);
; }
; template <int MODE>
; __device__ __forceinline__ void attn_pass(const bf16_t* __restrict__ Qb, const bf16_t* __restrict__ Kh, const bf16_t* __restrict__ Vh, const int NT, const int kr0, const int g4, const int map,
;                                           LAS unsigned char* lds, f32x16 (&o)[4]) {
;     ...
;         pv_d0(o, vb0 + SHM_V, pa0, pa1, pa2, pa3); partialSM<MODE>(pA0, pA1, m_reg, mnA, alA);
;         __syncthreads(); SWAIT(); SWRITE(1, SO);
;         RESC(alA); __syncthreads();
.LBB0_477:
	ds_read_b64_tr_b16 v[228:229], v173 offset:0
	ds_read_b64_tr_b16 v[230:231], v173 offset:0x800
	ds_read_b64_tr_b16 v[232:233], v173 offset:0x1000
	ds_read_b64_tr_b16 v[234:235], v173 offset:0x1800
	ds_read_b64_tr_b16 v[236:237], v173 offset:0x2000
	ds_read_b64_tr_b16 v[238:239], v173 offset:0x2800
	ds_read_b64_tr_b16 v[240:241], v173 offset:0x3000
	ds_read_b64_tr_b16 v[242:243], v173 offset:0x3800
	s_waitcnt lgkmcnt(0)
	s_nop 0
	v_mfma_f32_32x32x16_bf16 v[2:17], v[68:71], v[228:231], v[2:17]
	ds_read_b64_tr_b16 v[228:229], v173 offset:0x200
	ds_read_b64_tr_b16 v[230:231], v173 offset:0xa00
	v_mfma_f32_32x32x16_bf16 v[2:17], v[76:79], v[232:235], v[2:17]
	ds_read_b64_tr_b16 v[232:233], v173 offset:0x1200
	ds_read_b64_tr_b16 v[234:235], v173 offset:0x1a00
	v_mfma_f32_32x32x16_bf16 v[2:17], v[166:169], v[236:239], v[2:17]
	ds_read_b64_tr_b16 v[236:237], v173 offset:0x2200
	ds_read_b64_tr_b16 v[238:239], v173 offset:0x2a00
	ds_read_b64_tr_b16 v[244:245], v173 offset:0x3200
	ds_read_b64_tr_b16 v[246:247], v173 offset:0x3a00
	s_waitcnt lgkmcnt(0)
	v_mfma_f32_32x32x16_bf16 v[2:17], v[162:165], v[240:243], v[2:17]
	v_mfma_f32_32x32x16_bf16 v[50:65], v[68:71], v[228:231], v[50:65]
	ds_read_b64_tr_b16 v[228:229], v173 offset:0x400
	ds_read_b64_tr_b16 v[230:231], v173 offset:0xc00
	v_mfma_f32_32x32x16_bf16 v[50:65], v[76:79], v[232:235], v[50:65]
	ds_read_b64_tr_b16 v[232:233], v173 offset:0x1400
	ds_read_b64_tr_b16 v[234:235], v173 offset:0x1c00
	v_mfma_f32_32x32x16_bf16 v[50:65], v[166:169], v[236:239], v[50:65]
	ds_read_b64_tr_b16 v[236:237], v173 offset:0x2400
	ds_read_b64_tr_b16 v[238:239], v173 offset:0x2c00
	ds_read_b64_tr_b16 v[240:241], v173 offset:0x3400
	ds_read_b64_tr_b16 v[242:243], v173 offset:0x3c00
	s_waitcnt lgkmcnt(0)
	v_mfma_f32_32x32x16_bf16 v[50:65], v[162:165], v[244:247], v[50:65]
	v_mfma_f32_32x32x16_bf16 v[34:49], v[68:71], v[228:231], v[34:49]
	ds_read_b64_tr_b16 v[228:229], v173 offset:0x600
	ds_read_b64_tr_b16 v[230:231], v173 offset:0xe00
	v_mfma_f32_32x32x16_bf16 v[34:49], v[76:79], v[232:235], v[34:49]
	ds_read_b64_tr_b16 v[232:233], v173 offset:0x1600
	ds_read_b64_tr_b16 v[234:235], v173 offset:0x1e00
	v_mfma_f32_32x32x16_bf16 v[34:49], v[166:169], v[236:239], v[34:49]
	ds_read_b64_tr_b16 v[236:237], v173 offset:0x2600
	ds_read_b64_tr_b16 v[238:239], v173 offset:0x2e00
	ds_read_b64_tr_b16 v[244:245], v173 offset:0x3600
	ds_read_b64_tr_b16 v[246:247], v173 offset:0x3e00
	s_waitcnt lgkmcnt(0)
	v_mfma_f32_32x32x16_bf16 v[34:49], v[162:165], v[240:243], v[34:49]
	v_mfma_f32_32x32x16_bf16 v[18:33], v[68:71], v[228:231], v[18:33]
	v_max_f32_e32 v75, v83, v83
	v_max_f32_e32 v80, v82, v82
	v_max_f32_e32 v75, v80, v75
	v_max3_f32 v75, v75, v84, v85
	v_max3_f32 v75, v75, v86, v87
	v_max3_f32 v68, v75, v88, v89
	v_max3_f32 v68, v68, v90, v91
	v_max3_f32 v68, v68, v92, v93
	v_mfma_f32_32x32x16_bf16 v[18:33], v[76:79], v[232:235], v[18:33]
	v_max3_f32 v68, v68, v94, v95
	v_max3_f32 v68, v68, v96, v97
	v_max3_f32 v66, v68, v66, v99
	v_max3_f32 v66, v66, v100, v101
	v_max3_f32 v66, v66, v102, v103
	v_max3_f32 v66, v66, v104, v73
	v_max3_f32 v66, v66, v74, v107
	v_max3_f32 v66, v66, v108, v109
	v_mfma_f32_32x32x16_bf16 v[18:33], v[166:169], v[236:239], v[18:33]
	v_max3_f32 v66, v66, v110, v111
	v_max3_f32 v66, v66, v112, v81
	v_mov_b32_e32 v68, v66
	s_nop 1
	v_permlane32_swap_b32_e32 v66, v68
	v_max_f32_e32 v68, v68, v68
	v_max_f32_e32 v66, v66, v66
	v_max_f32_e32 v66, v66, v68
	v_max_f32_e32 v69, v226, v226
	v_sub_f32_e32 v68, v66, v226
	v_max_f32_e32 v66, v69, v66
	v_mfma_f32_32x32x16_bf16 v[18:33], v[162:165], v[244:247], v[18:33]
	v_sub_f32_e32 v69, v226, v66
	v_mul_f32_e32 v69, 0x3e0293ee, v69
	v_exp_f32_e32 v69, v69
	v_cmp_ge_f32_e32 vcc, s7, v68
	s_cmp_eq_u64 vcc, exec
	s_cselect_b64 s[4:5], -1, 0
	s_waitcnt vmcnt(0)
	ds_write_b128 v192, v[154:157] offset:49152
	ds_write_b128 v193, v[158:161] offset:49152
	s_waitcnt lgkmcnt(0)
	s_barrier
	s_waitcnt vmcnt(4)
	v_cndmask_b32_e64 v98, v69, 1.0, s[4:5]
	v_cmp_gt_f32_e32 vcc, 1.0, v98
	s_waitcnt vmcnt(3)
	ds_write_b128 v199, v[146:149] offset:16384
	s_waitcnt vmcnt(2)
	ds_write_b128 v200, v[150:153] offset:16384
	s_waitcnt vmcnt(1)
	s_waitcnt vmcnt(0)
	s_cbranch_vccz .LBB0_481
	s_and_saveexec_b64 s[44:45], s[0:1]
	ds_write_b32 v171, v98 offset:128
	s_or_b64 exec, exec, s[44:45]
	s_waitcnt lgkmcnt(0)
	ds_read_b128 v[68:71], v207 offset:224
	ds_read_b128 v[74:77], v207 offset:192
	ds_read_b128 v[100:103], v207 offset:160
	ds_read_b128 v[104:107], v207 offset:128
	s_waitcnt lgkmcnt(3)
	v_pk_mul_f32 v[16:17], v[16:17], v[70:71]
	s_waitcnt lgkmcnt(2)
	v_pk_mul_f32 v[12:13], v[12:13], v[76:77]
	s_waitcnt lgkmcnt(1)
	v_pk_mul_f32 v[8:9], v[8:9], v[102:103]
	s_waitcnt lgkmcnt(0)
	v_pk_mul_f32 v[4:5], v[4:5], v[106:107]
	v_pk_mul_f32 v[14:15], v[14:15], v[68:69]
	v_pk_mul_f32 v[10:11], v[10:11], v[74:75]
	v_pk_mul_f32 v[6:7], v[6:7], v[100:101]
	v_pk_mul_f32 v[2:3], v[2:3], v[104:105]
	v_pk_mul_f32 v[64:65], v[64:65], v[70:71]
	v_pk_mul_f32 v[60:61], v[60:61], v[76:77]
	v_pk_mul_f32 v[56:57], v[56:57], v[102:103]
	v_pk_mul_f32 v[52:53], v[52:53], v[106:107]
	v_pk_mul_f32 v[62:63], v[62:63], v[68:69]
	v_pk_mul_f32 v[58:59], v[58:59], v[74:75]
	v_pk_mul_f32 v[54:55], v[54:55], v[100:101]
	v_pk_mul_f32 v[50:51], v[50:51], v[104:105]
	v_pk_mul_f32 v[48:49], v[48:49], v[70:71]
	v_pk_mul_f32 v[44:45], v[44:45], v[76:77]
	v_pk_mul_f32 v[40:41], v[40:41], v[102:103]
	v_pk_mul_f32 v[36:37], v[36:37], v[106:107]
	v_pk_mul_f32 v[46:47], v[46:47], v[68:69]
	v_pk_mul_f32 v[42:43], v[42:43], v[74:75]
	v_pk_mul_f32 v[38:39], v[38:39], v[100:101]
	v_pk_mul_f32 v[34:35], v[34:35], v[104:105]
	v_pk_mul_f32 v[32:33], v[32:33], v[70:71]
	v_pk_mul_f32 v[28:29], v[28:29], v[76:77]
	v_pk_mul_f32 v[24:25], v[24:25], v[102:103]
	v_pk_mul_f32 v[20:21], v[20:21], v[106:107]
	v_pk_mul_f32 v[30:31], v[30:31], v[68:69]
	v_pk_mul_f32 v[26:27], v[26:27], v[74:75]
	v_pk_mul_f32 v[22:23], v[22:23], v[100:101]
	v_pk_mul_f32 v[18:19], v[18:19], v[104:105]
; #define SWAIT() do { if constexpr (MODE == 1) asm volatile("s_waitcnt vmcnt(3)" ::: "memory"); else asm volatile("s_waitcnt vmcnt(4)" ::: "memory"); } while (0)
; #define RESC(a) do { if (__any((a) < 1.f)) { if (hi == 0) al_l[r32] = (a); asm volatile("s_waitcnt lgkmcnt(0)" ::: "memory"); \
;     _Pragma("unroll") for (int d = 0; d < 4; ++d) _Pragma("unroll") for (int r = 0; r < 16; ++r) o[d][r] *= al_l[crow(r, hi)]; } } while (0)
; template <int MODE>
; __device__ __forceinline__ void partialSM(f32x16& p0, f32x16& p1, float& m_reg, float& mn, float& alpha) {
;     ...
;     const float mnC = -mn * C;
; #pragma unroll
;     for (int r = 0; r < 16; ++r) p0[r] = fmaf(p0[r], C, mnC);
; #pragma unroll
;     for (int r = 0; r < 16; ++r) p1[r] = fmaf(p1[r], C, mnC);
; #pragma unroll
;     for (int r = 0; r < 16; ++r) p0[r] = __builtin_amdgcn_exp2f(p0[r]);
; }
; template <int MODE>
; __device__ __forceinline__ void attn_pass(const bf16_t* __restrict__ Qb, const bf16_t* __restrict__ Kh, const bf16_t* __restrict__ Vh, const int NT, const int kr0, const int g4, const int map,
;                                           LAS unsigned char* lds, f32x16 (&o)[4]) {
;     ...
;         pv_d0(o, vb0 + SHM_V, pa0, pa1, pa2, pa3); partialSM<MODE>(pA0, pA1, m_reg, mnA, alA);
;         __syncthreads(); SWAIT(); SWRITE(1, SO);
;         RESC(alA); __syncthreads();
;     }
.LBB0_481:
	v_cndmask_b32_e64 v164, v66, v226, s[4:5]
	v_mul_f32_e32 v66, 0xbe0293ee, v164
	v_fmamk_f32 v71, v85, 0x3e0293ee, v66
	v_mov_b32_e32 v85, v66
	v_fmamk_f32 v68, v82, 0x3e0293ee, v66
	v_fmamk_f32 v69, v83, 0x3e0293ee, v66
	v_fmamk_f32 v70, v84, 0x3e0293ee, v66
	v_fmamk_f32 v73, v86, 0x3e0293ee, v66
	v_fmamk_f32 v74, v87, 0x3e0293ee, v66
	v_fmamk_f32 v75, v88, 0x3e0293ee, v66
	v_fmamk_f32 v76, v89, 0x3e0293ee, v66
	v_fmamk_f32 v77, v90, 0x3e0293ee, v66
	v_fmamk_f32 v78, v91, 0x3e0293ee, v66
	v_fmamk_f32 v79, v92, 0x3e0293ee, v66
	v_fmamk_f32 v80, v93, 0x3e0293ee, v66
	v_fmamk_f32 v82, v94, 0x3e0293ee, v66
	v_fmamk_f32 v83, v95, 0x3e0293ee, v66
	v_fmamk_f32 v84, v96, 0x3e0293ee, v66
	v_fmac_f32_e32 v85, 0x3e0293ee, v97
	v_exp_f32_e32 v234, v68
	v_exp_f32_e32 v236, v69
	v_exp_f32_e32 v232, v70
	v_exp_f32_e32 v235, v71
	v_exp_f32_e32 v230, v73
	v_exp_f32_e32 v233, v74
	v_exp_f32_e32 v229, v75
	v_exp_f32_e32 v231, v76
	v_exp_f32_e32 v226, v77
	v_exp_f32_e32 v228, v78
	v_exp_f32_e32 v168, v79
	v_exp_f32_e32 v227, v80
	v_exp_f32_e32 v166, v82
	v_exp_f32_e32 v169, v83
	v_exp_f32_e32 v165, v84
	v_exp_f32_e32 v167, v85
	v_mov_b32_e32 v129, v81
	v_pk_fma_f32 v[156:157], v[114:115], s[40:41], v[66:67] op_sel_hi:[1,0,0]
	v_pk_fma_f32 v[154:155], v[116:117], s[40:41], v[66:67] op_sel_hi:[1,0,0]
	v_pk_fma_f32 v[152:153], v[118:119], s[40:41], v[66:67] op_sel_hi:[1,0,0]
	v_pk_fma_f32 v[150:151], v[120:121], s[40:41], v[66:67] op_sel_hi:[1,0,0]
	v_pk_fma_f32 v[148:149], v[122:123], s[40:41], v[66:67] op_sel_hi:[1,0,0]
	v_pk_fma_f32 v[146:147], v[124:125], s[40:41], v[66:67] op_sel_hi:[1,0,0]
	v_pk_fma_f32 v[162:163], v[126:127], s[40:41], v[66:67] op_sel_hi:[1,0,0]
	v_pk_fma_f32 v[160:161], v[128:129], s[40:41], v[66:67] op_sel_hi:[1,0,0]
	v_add_f32_e32 v66, v113, v224
	v_fmac_f32_e32 v66, v220, v188
	v_add_f32_e32 v188, v67, v72
	v_fmac_f32_e32 v188, v66, v225
	s_add_i32 s6, s6, 2
	v_lshl_add_u64 v[180:181], v[180:181], 0, s[20:21]
	s_addk_i32 s3, 0x80
	s_and_b64 vcc, exec, s[42:43]
	s_waitcnt lgkmcnt(0)
	s_cbranch_vccnz .LBB0_483
	v_mov_b32_e32 v220, v98
	s_branch .LBB0_460
